# v4b: GLA-scan conversion tiles partly moved to WGs pulled out of in0/in1 GEMM phases; flat->global nt; counted vmcnt in GLA loop
# speedup vs baseline: 1.0076x; 1.0076x over previous
;     __device__ bool next(int i, Unit& u) const {
;         const long L = (long)i * G + c; if (L >= nwg) return false;
;         int wgid = (int)L; { const int q = nwg / NXCD, r = nwg % NXCD, xcd = wgid % NXCD, off = wgid / NXCD; wgid = (xcd < r ? xcd * (q + 1) : r * (q + 1) + (xcd - r) * q) + off; }
;         const int nig = WGM * nN, gid = wgid / nig, fm = gid * WGM, gsz = (nM - fm) < WGM ? (nM - fm) : WGM;
;         u.pm = fm + ((wgid % nig) % gsz); u.pn = (wgid % nig) / gsz; u.k0 = 0; return true;
;     }
; template <class Epi, class Sched, bool ALIGN_EPI = false, bool SP2 = false>
; __device__ __forceinline__ void gemm_phase(PG8_LAS unsigned char* lds, const Gemm g, const Sched& S, const Epi& E) {
;     const int tid = ptid(), wid = __builtin_amdgcn_readfirstlane(tid >> 6), lane = tid & 63, wr = wid >> 2, wc = wid & 3, fr = lane & 15, fq = lane >> 4;
;     const int K = g.K, nt = K / BK, LD = g.ld;
;     unsigned voffA[2], voffB[2];
; #pragma unroll
;     for (int i = 0; i < 2; ++i) { int R, C; stage_rc(tid * 16 + i * 8192, R, C); const int Rb = Epi::PERM ? ((R & ~31) + perm32(R & 31)) : R;
;         voffA[i] = (unsigned)(R * LD + C) * 2u; voffB[i] = (unsigned)(Rb * LD + C) * 2u; }
;     const size_t kstep = (size_t)(BK * 2);
;     const size_t hstep = (size_t)HALF * LD * 2;
;     const size_t tstep = 2 * hstep;
;     const unsigned ldsw = (unsigned)wid * 1024u;
;     const int aoff = lds_byte(wr * 64 + fr, fq * 8), boff = lds_byte(wc * 32 + fr, fq * 8);
;     ...
;     Unit cur, nxt; int ui = 0;
;     if (!S.next(0, cur)) return;
;     f32x4 acc[2][2][4][2];
; #pragma unroll
;     for (int a = 0; a < 2; ++a)
; #pragma unroll
;         for (int b = 0; b < 2; ++b)
; #pragma unroll
;             for (int m = 0; m < 4; ++m)
; #pragma unroll
;                 for (int n = 0; n < 2; ++n) acc[a][b][m][n] = (f32x4){0.f, 0.f, 0.f, 0.f};
;     bf16x8 At[4][2], B0[2][2], B1[2][2];
;     const char* cA = (const char*)g.A + (size_t)cur.pm * tstep + (size_t)cur.k0 * 2; const char* cB = (const char*)g.Bt + (size_t)cur.pn * tstep + (size_t)cur.k0 * 2;
;     S.a_ready(cur);
;     if constexpr (SP2) {
;         PG8_STAGE(PG8_SB(0, 0), cB, voffB); PG8_STAGE(PG8_SB(0, 1), cB + hstep, voffB); PG8_STAGE(PG8_SA(0, 0), cA, voffA); PG8_STAGE(PG8_SA(0, 1), cA + hstep, voffA);
;         if (wr == 1) PG8_BAR;
;         PG8_WAIT_V(2); PG8_BAR;
.LBB0_217:
	v_writelane_b32 v248, s33, 38
	s_or_b64 exec, exec, s[0:1]
	s_ashr_i32 s97, s96, 31
	s_ashr_i32 s91, s90, 31
	v_mov_b32_e32 v11, v0
	s_waitcnt lgkmcnt(0)
	s_barrier
	s_cmpk_lt_i32 s90, 0xe0
	s_mov_b64 s[76:77], s[96:97]
	v_readfirstlane_b32 s1, v11
	v_writelane_b32 v248, s90, 39
	s_nop 1
	v_writelane_b32 v248, s91, 40
	s_cbranch_scc0 .Lcv0_start
	v_lshlrev_b32_e32 v2, 4, v11
	v_add_u32_e32 v3, 0x2000, v2
	v_ashrrev_i32_e32 v4, 31, v3
	v_lshrrev_b32_e32 v4, 22, v4
	v_add_u32_e32 v4, v3, v4
	v_ashrrev_i32_e32 v10, 10, v4
	v_mul_i32_i24_e32 v4, 0x400, v10
	v_sub_u32_e32 v3, v3, v4
	v_lshrrev_b32_e32 v4, 4, v3
	v_bitop3_b32 v3, v4, v3, 32 bitop3:0x6c
	v_ashrrev_i32_e32 v4, 31, v3
	v_lshrrev_b32_e32 v4, 26, v4
	v_add_u32_e32 v4, v3, v4
	v_lshlrev_b32_e32 v5, 3, v10
	v_ashrrev_i32_e32 v12, 6, v4
	v_and_b32_e32 v5, -16, v5
	v_add_u32_e32 v5, v12, v5
	v_and_b32_e32 v6, 3, v12
	s_mov_b32 s0, 0xfffe0
	v_lshrrev_b32_e32 v7, 2, v5
	v_lshlrev_b32_e32 v8, 1, v5
	v_and_b32_e32 v4, 0xc0, v4
	v_and_or_b32 v6, v5, s0, v6
	v_and_b32_e32 v7, 4, v7
	v_and_b32_e32 v8, 24, v8
	v_sub_u32_e32 v3, v3, v4
	v_mov_b32_e32 v4, 1
	v_or3_b32 v6, v6, v7, v8
	v_lshlrev_b32_e32 v7, 5, v10
	v_ashrrev_i16_sdwa v3, v4, sext(v3) dst_sel:DWORD dst_unused:UNUSED_PAD src0_sel:DWORD src1_sel:BYTE_0
	v_and_b32_e32 v7, 32, v7
	v_bfe_i32 v13, v3, 0, 16
	v_add_lshl_u32 v3, v7, v13, 1
	v_lshl_add_u32 v130, v6, 12, v3
	v_lshl_add_u32 v132, v5, 12, v3
	v_bfe_i32 v3, v11, 27, 1
	v_lshrrev_b32_e32 v3, 22, v3
	v_add_u32_e32 v3, v2, v3
	v_and_b32_e32 v3, 0xfffffc00, v3
	v_sub_u32_e32 v2, v2, v3
	v_lshrrev_b32_e32 v3, 4, v2
	v_bitop3_b32 v3, v3, v2, 32 bitop3:0x6c
	v_ashrrev_i32_e32 v2, 31, v2
	v_lshrrev_b32_e32 v2, 26, v2
	v_add_u32_e32 v2, v3, v2
	v_ashrrev_i32_e32 v14, 6, v2
	v_ashrrev_i32_e32 v2, 31, v11
	v_lshrrev_b32_e32 v2, 26, v2
	v_add_u32_e32 v2, v11, v2
	v_ashrrev_i32_e32 v15, 6, v2
	v_lshlrev_b32_e32 v2, 3, v15
	v_and_b32_e32 v2, -16, v2
	v_add_u32_e32 v2, v14, v2
	v_and_b32_e32 v5, 3, v14
	v_and_or_b32 v5, v2, s0, v5
	s_lshr_b32 s0, s91, 29
	s_add_i32 s0, s90, s0
	s_and_b32 s3, s0, -8
	s_sub_i32 s3, s90, s3
	s_ashr_i32 s6, s1, 6
	s_mul_i32 s5, s3, 0x6e
	s_ashr_i32 s8, s1, 8
	s_lshl_b32 s2, s6, 10
	s_add_i32 s5, s5, 4
	s_ashr_i32 s0, s0, 3
	s_mul_i32 s4, s3, 0x6f
	s_cmp_lt_i32 s3, 4
	s_cselect_b32 s3, s4, s5
	v_lshrrev_b32_e32 v6, 2, v2
	v_lshlrev_b32_e32 v7, 1, v2
	s_add_i32 s3, s3, s0
	v_and_b32_e32 v6, 4, v6
	v_and_b32_e32 v7, 24, v7
	s_mul_hi_i32 s0, s3, 0x4ec4ec4f
	v_or3_b32 v5, v5, v6, v7
	v_mul_i32_i24_e32 v7, 64, v14
	s_lshr_b32 s4, s0, 31
	s_ashr_i32 s0, s0, 6
	v_sub_u32_e32 v3, v3, v7
	s_add_i32 s0, s0, s4
	v_lshlrev_b32_e32 v6, 5, v15
	v_ashrrev_i16_sdwa v3, v4, sext(v3) dst_sel:DWORD dst_unused:UNUSED_PAD src0_sel:DWORD src1_sel:BYTE_0
	s_lshl_b32 s7, s0, 3
	v_and_b32_e32 v6, 32, v6
	v_bfe_i32 v16, v3, 0, 16
	s_sub_i32 s4, 34, s7
	s_mulk_i32 s0, 0xd0
	v_add_lshl_u32 v3, v6, v16, 1
	s_min_u32 s9, s4, 8
	s_sub_i32 s3, s3, s0
	v_lshl_add_u32 v134, v5, 12, v3
	s_sext_i32_i16 s0, s3
	v_cvt_f32_ubyte0_e32 v5, s9
	v_cvt_f32_i32_e32 v4, s0
	v_rcp_iflag_f32_e32 v6, v5
	v_lshl_add_u32 v136, v2, 12, v3
	s_ashr_i32 s0, s0, 30
	s_or_b32 s0, s0, 1
	v_mul_f32_e32 v2, v4, v6
	v_trunc_f32_e32 v2, v2
	v_fma_f32 v3, -v2, v5, v4
	v_cvt_i32_f32_e32 v2, v2
	v_cmp_ge_f32_e64 s[4:5], |v3|, v5
	s_and_b64 s[4:5], s[4:5], exec
	s_cselect_b32 s0, s0, 0
	v_readfirstlane_b32 s4, v2
	s_add_i32 s0, s4, s0
	s_mul_i32 s4, s0, s9
	s_sub_i32 s3, s3, s4
	s_sext_i32_i16 s3, s3
	s_add_i32 s10, s7, s3
	s_ashr_i32 s11, s10, 31
	s_bfe_i64 s[12:13], s[0:1], 0x100000
	v_readlane_b32 s56, v246, 0
	s_lshl_b64 s[4:5], s[10:11], 20
	s_lshl_b64 s[12:13], s[12:13], 20
	v_readlane_b32 s58, v246, 2
	v_readlane_b32 s59, v246, 3
	s_add_u32 s28, s58, s12
	s_addc_u32 s29, s59, s13
	s_add_i32 s3, s2, 0
	s_add_i32 m0, s3, 0x10000
	v_readlane_b32 s57, v246, 1
	global_load_lds_dwordx4 v134, s[28:29]
	s_add_i32 m0, s3, 0x12000
	v_readlane_b32 s60, v246, 4
	v_readlane_b32 s61, v246, 5
	v_readlane_b32 s62, v246, 6
	v_readlane_b32 s63, v246, 7
	v_readlane_b32 s64, v246, 8
	v_readlane_b32 s65, v246, 9
	v_readlane_b32 s66, v246, 10
	v_readlane_b32 s67, v246, 11
	v_readlane_b32 s68, v246, 12
	v_readlane_b32 s69, v246, 13
	v_readlane_b32 s70, v246, 14
	v_readlane_b32 s71, v246, 15
	s_add_u32 s12, s28, 0x80000
	global_load_lds_dwordx4 v130, s[28:29]
	s_addc_u32 s13, s29, 0
	s_add_i32 m0, s3, 0x14000
	v_readlane_b32 s56, v247, 16
	global_load_lds_dwordx4 v134, s[12:13]
	s_add_i32 m0, s3, 0x16000
	v_readlane_b32 s64, v247, 24
	v_readlane_b32 s65, v247, 25
	s_add_u32 s26, s64, s4
	s_addc_u32 s27, s65, s5
	s_add_i32 s11, s3, 0x2000
	global_load_lds_dwordx4 v130, s[12:13]
	s_mov_b32 m0, s3
	s_add_u32 s4, s26, 0x80000
	global_load_lds_dwordx4 v136, s[26:27]
	s_mov_b32 m0, s11
	s_addc_u32 s5, s27, 0
	s_add_i32 s33, s3, 0x4000
	global_load_lds_dwordx4 v132, s[26:27]
	s_mov_b32 m0, s33
	s_add_i32 s36, s3, 0x6000
	global_load_lds_dwordx4 v136, s[4:5]
	s_mov_b32 m0, s36
	v_mov_b32_e32 v135, 0
	global_load_lds_dwordx4 v132, s[4:5]
	s_cmp_eq_u32 s8, 1
	v_mov_b32_e32 v131, v135
	v_mov_b32_e32 v137, v135
	v_mov_b32_e32 v133, v135
	s_cselect_b64 s[4:5], -1, 0
	s_mov_b32 s37, 0
	v_lshl_add_u64 v[6:7], s[28:29], 0, v[134:135]
	v_lshl_add_u64 v[4:5], s[28:29], 0, v[130:131]
	v_lshl_add_u64 v[2:3], s[26:27], 0, v[136:137]
	v_writelane_b32 v248, s4, 45
	s_cmp_lg_u32 s8, 1
	v_lshl_add_u64 v[8:9], s[26:27], 0, v[132:133]
	v_readlane_b32 s57, v247, 17
	v_readlane_b32 s58, v247, 18
	v_readlane_b32 s59, v247, 19
	v_readlane_b32 s60, v247, 20
	v_readlane_b32 s61, v247, 21
	v_readlane_b32 s62, v247, 22
	v_readlane_b32 s63, v247, 23
	v_readlane_b32 s66, v247, 26
	v_readlane_b32 s67, v247, 27
	v_readlane_b32 s68, v247, 28
	v_readlane_b32 s69, v247, 29
	v_readlane_b32 s70, v247, 30
	v_readlane_b32 s71, v247, 31
	v_writelane_b32 v248, s5, 46
	s_cbranch_scc1 .LBB0_220
	s_barrier

;     __device__ bool next(int i, Unit& u) const {
;         const long L = (long)i * G + c; if (L >= nwg) return false;
;         int wgid = (int)L; { const int q = nwg / NXCD, r = nwg % NXCD, xcd = wgid % NXCD, off = wgid / NXCD; wgid = (xcd < r ? xcd * (q + 1) : r * (q + 1) + (xcd - r) * q) + off; }
;         const int nig = WGM * nN, gid = wgid / nig, fm = gid * WGM, gsz = (nM - fm) < WGM ? (nM - fm) : WGM;
;         u.pm = fm + ((wgid % nig) % gsz); u.pn = (wgid % nig) / gsz; u.k0 = 0; return true;
; template <class Epi, class Sched, bool ALIGN_EPI = false, bool SP2 = false>
; __device__ __forceinline__ void gemm_phase(PG8_LAS unsigned char* lds, const Gemm g, const Sched& S, const Epi& E) {
;     ...
;         const bool has_next = S.next(ui + 1, nxt);
.LBB0_223:
	s_add_i32 s37, s37, 1
	s_mul_i32 s0, s37, s97
	s_mul_hi_u32 s1, s37, 0xe0
	s_add_i32 s1, s1, s0
	s_mul_i32 s0, s37, 0xe0
	s_add_u32 s16, s0, s90
	s_addc_u32 s17, s1, s91
	v_cmp_gt_i64_e32 vcc, s[16:17], v[144:145]
	v_cmp_lt_i64_e64 s[0:1], s[16:17], v[142:143]
	s_cbranch_vccnz .LBB0_229
	s_ashr_i32 s12, s16, 31
	s_lshr_b32 s12, s12, 29
	s_add_i32 s14, s16, s12
	s_and_b32 s12, s14, -8
	s_sub_i32 s15, s16, s12
	s_cmp_gt_i32 s15, 3
	s_mov_b64 s[12:13], -1
	s_cbranch_scc0 .LBB0_226
	s_mul_i32 s12, s15, 0x6e
	s_add_i32 s16, s12, 4
	s_mov_b64 s[12:13], 0

; __device__ __forceinline__ ConvTile conv_tile_desc(const unsigned long long* tab, int t) {
;     ...
;     else { const int u = (t < CT_TOTAL ? t : CT_TOTAL - 1) - CT_C; e = u / 7168; const int v = u % 7168; si = 9; di = 17; N = DM; K = EXD; nb = v & 31; kb = v >> 5; }
;     const int n0 = nb * 64;
;     int col0 = n0, nvalid = 64;
;     if (mode) { col0 = (n0 >> 8) * 128 + (n0 & 127); si += (n0 >> 7) & 1; }
;     if (npad) { nvalid = N - n0; if (nvalid <= 0) col0 = 0; }
;     ConvTile c;
;     const size_t KN = (size_t)K * N;
;     c.src = (const float*)tab[si] + (size_t)e * KN + (size_t)(kb * 32) * N + col0;
;     c.dst = (bf16_t*)tab[di] + (size_t)e * (mode ? 2 * KN : KN) + (size_t)n0 * K + kb * 32;
;     c.N = N; c.K = K; c.nvalid = nvalid;
;     return c;
; }
.Lcv0_start:
	v_and_b32_e32 v96, 63, v0
	v_lshrrev_b32_e32 v97, 6, v0
	v_lshrrev_b32_e32 v98, 4, v96
	v_and_b32_e32 v99, 15, v96
	v_readfirstlane_b32 s2, v97
	v_lshlrev_b32_e32 v100, 16, v98
	v_lshl_add_u32 v100, v99, 4, v100
	v_add_u32_e32 v101, 0x2000, v100
	v_add_u32_e32 v102, 0x4000, v100
	v_add_u32_e32 v103, 0x6000, v100
	v_add_u32_e32 v104, 0x8000, v100
	v_add_u32_e32 v105, 0xa000, v100
	v_add_u32_e32 v106, 0xc000, v100
	v_add_u32_e32 v107, 0xe000, v100
	v_mul_u32_u24_e32 v108, 0xe000, v99
	v_lshl_add_u32 v108, v98, 4, v108
	v_add_u32_e32 v109, 0x3800, v108
	v_add_u32_e32 v110, 0x7000, v108
	v_add_u32_e32 v111, 0xa800, v108
	v_mov_b32_e32 v112, 0x20088
	v_mov_b32_e32 v113, 0x200c8
	ds_read_b64 v[114:115], v112
	ds_read_b64 v[116:117], v113
	s_waitcnt lgkmcnt(0)
	v_readfirstlane_b32 s4, v114
	v_readfirstlane_b32 s5, v115
	v_readfirstlane_b32 s6, v116
	v_readfirstlane_b32 s7, v117
	s_sub_i32 s3, s90, 224
	s_lshl_b32 s3, s3, 3
	s_add_i32 s3, s3, s2
	s_add_i32 s3, s3, 0x2ac00
	s_nop 4
	s_min_u32 s12, s3, 0x324ff
	s_sub_u32 s12, s12, 0x24500
	s_lshr_b32 s13, s12, 10
	s_mul_i32 s13, s13, 37
	s_lshr_b32 s13, s13, 8
	s_mul_i32 s28, s13, 0x1c00
	s_sub_u32 s12, s12, s28
	s_and_b32 s28, s12, 31
	s_lshr_b32 s12, s12, 5
	s_mul_i32 s29, s13, 0x3800000
	s_lshl_b32 s32, s12, 18
	s_add_u32 s29, s29, s32
	s_lshl_b32 s32, s28, 8
	s_add_u32 s29, s29, s32
	s_add_u32 s8, s4, s29
	s_addc_u32 s9, s5, 0
	s_mul_i32 s29, s13, 0x1c00000
	s_mul_i32 s32, s28, 0xe0000
	s_add_u32 s29, s29, s32
	s_lshl_b32 s32, s12, 6
	s_add_u32 s29, s29, s32
	s_add_u32 s10, s6, s29
	s_addc_u32 s11, s7, 0
	s_nop 0
	global_load_dwordx4 v[128:131], v100, s[8:9] nt
	global_load_dwordx4 v[132:135], v101, s[8:9] nt
	global_load_dwordx4 v[136:139], v102, s[8:9] nt
	global_load_dwordx4 v[140:143], v103, s[8:9] nt
	global_load_dwordx4 v[144:147], v104, s[8:9] nt
	global_load_dwordx4 v[148:151], v105, s[8:9] nt
	global_load_dwordx4 v[152:155], v106, s[8:9] nt
	global_load_dwordx4 v[156:159], v107, s[8:9] nt
	s_add_i32 s3, s3, 256
	s_min_u32 s12, s3, 0x324ff
	s_sub_u32 s12, s12, 0x24500
	s_lshr_b32 s13, s12, 10
	s_mul_i32 s13, s13, 37
	s_lshr_b32 s13, s13, 8
	s_mul_i32 s28, s13, 0x1c00
	s_sub_u32 s12, s12, s28
	s_and_b32 s28, s12, 31
	s_lshr_b32 s12, s12, 5
	s_mul_i32 s29, s13, 0x3800000
	s_lshl_b32 s32, s12, 18
	s_add_u32 s29, s29, s32
	s_lshl_b32 s32, s28, 8
	s_add_u32 s29, s29, s32
	s_add_u32 s8, s4, s29
	s_addc_u32 s9, s5, 0
	s_mul_i32 s29, s13, 0x1c00000
	s_mul_i32 s32, s28, 0xe0000
	s_add_u32 s29, s29, s32
	s_lshl_b32 s32, s12, 6
	s_add_u32 s29, s29, s32
	s_add_u32 s36, s6, s29
	s_addc_u32 s37, s7, 0
	s_nop 0
	global_load_dwordx4 v[64:67], v100, s[8:9] nt
	global_load_dwordx4 v[68:71], v101, s[8:9] nt
	global_load_dwordx4 v[72:75], v102, s[8:9] nt
	global_load_dwordx4 v[76:79], v103, s[8:9] nt
	global_load_dwordx4 v[80:83], v104, s[8:9] nt
	global_load_dwordx4 v[84:87], v105, s[8:9] nt
	global_load_dwordx4 v[88:91], v106, s[8:9] nt
	global_load_dwordx4 v[92:95], v107, s[8:9] nt
	s_waitcnt vmcnt(8)
	v_cvt_pk_bf16_f32 v112, v128, v132
	v_cvt_pk_bf16_f32 v113, v136, v140
	v_cvt_pk_bf16_f32 v114, v144, v148
	v_cvt_pk_bf16_f32 v115, v152, v156
	global_store_dwordx4 v108, v[112:115], s[10:11] nt
	v_cvt_pk_bf16_f32 v116, v129, v133
	v_cvt_pk_bf16_f32 v117, v137, v141
	v_cvt_pk_bf16_f32 v118, v145, v149
	v_cvt_pk_bf16_f32 v119, v153, v157
	global_store_dwordx4 v109, v[116:119], s[10:11] nt
	v_cvt_pk_bf16_f32 v120, v130, v134
	v_cvt_pk_bf16_f32 v121, v138, v142
	v_cvt_pk_bf16_f32 v122, v146, v150
	v_cvt_pk_bf16_f32 v123, v154, v158
	global_store_dwordx4 v110, v[120:123], s[10:11] nt
	v_cvt_pk_bf16_f32 v96, v131, v135
	v_cvt_pk_bf16_f32 v97, v139, v143
	v_cvt_pk_bf16_f32 v98, v147, v151
	v_cvt_pk_bf16_f32 v99, v155, v159
	global_store_dwordx4 v111, v[96:99], s[10:11] nt
	s_movk_i32 s33, 27
; __device__ __forceinline__ ConvTile conv_tile_desc(const unsigned long long* tab, int t) {
;     ...
;     else { const int u = (t < CT_TOTAL ? t : CT_TOTAL - 1) - CT_C; e = u / 7168; const int v = u % 7168; si = 9; di = 17; N = DM; K = EXD; nb = v & 31; kb = v >> 5; }
;     const int n0 = nb * 64;
;     int col0 = n0, nvalid = 64;
;     if (mode) { col0 = (n0 >> 8) * 128 + (n0 & 127); si += (n0 >> 7) & 1; }
;     if (npad) { nvalid = N - n0; if (nvalid <= 0) col0 = 0; }
;     ConvTile c;
;     const size_t KN = (size_t)K * N;
;     c.src = (const float*)tab[si] + (size_t)e * KN + (size_t)(kb * 32) * N + col0;
;     c.dst = (bf16_t*)tab[di] + (size_t)e * (mode ? 2 * KN : KN) + (size_t)n0 * K + kb * 32;
;     c.N = N; c.K = K; c.nvalid = nvalid;
;     return c;
; }
.Lcv0_loop:
	s_add_i32 s3, s3, 256
	s_min_u32 s12, s3, 0x324ff
	s_sub_u32 s12, s12, 0x24500
	s_lshr_b32 s13, s12, 10
	s_mul_i32 s13, s13, 37
	s_lshr_b32 s13, s13, 8
	s_mul_i32 s28, s13, 0x1c00
	s_sub_u32 s12, s12, s28
	s_and_b32 s28, s12, 31
	s_lshr_b32 s12, s12, 5
	s_mul_i32 s29, s13, 0x3800000
	s_lshl_b32 s32, s12, 18
	s_add_u32 s29, s29, s32
	s_lshl_b32 s32, s28, 8
	s_add_u32 s29, s29, s32
	s_add_u32 s8, s4, s29
	s_addc_u32 s9, s5, 0
	s_mul_i32 s29, s13, 0x1c00000
	s_mul_i32 s32, s28, 0xe0000
	s_add_u32 s29, s29, s32
	s_lshl_b32 s32, s12, 6
	s_add_u32 s29, s29, s32
	s_add_u32 s10, s6, s29
	s_addc_u32 s11, s7, 0
	s_nop 0
	global_load_dwordx4 v[128:131], v100, s[8:9] nt
	global_load_dwordx4 v[132:135], v101, s[8:9] nt
	global_load_dwordx4 v[136:139], v102, s[8:9] nt
	global_load_dwordx4 v[140:143], v103, s[8:9] nt
	global_load_dwordx4 v[144:147], v104, s[8:9] nt
	global_load_dwordx4 v[148:151], v105, s[8:9] nt
	global_load_dwordx4 v[152:155], v106, s[8:9] nt
	global_load_dwordx4 v[156:159], v107, s[8:9] nt
	s_waitcnt vmcnt(12)
	v_cvt_pk_bf16_f32 v112, v64, v68
	v_cvt_pk_bf16_f32 v113, v72, v76
	v_cvt_pk_bf16_f32 v114, v80, v84
	v_cvt_pk_bf16_f32 v115, v88, v92
	global_store_dwordx4 v108, v[112:115], s[36:37] nt
	v_cvt_pk_bf16_f32 v116, v65, v69
	v_cvt_pk_bf16_f32 v117, v73, v77
	v_cvt_pk_bf16_f32 v118, v81, v85
	v_cvt_pk_bf16_f32 v119, v89, v93
	global_store_dwordx4 v109, v[116:119], s[36:37] nt
	v_cvt_pk_bf16_f32 v120, v66, v70
	v_cvt_pk_bf16_f32 v121, v74, v78
	v_cvt_pk_bf16_f32 v122, v82, v86
	v_cvt_pk_bf16_f32 v123, v90, v94
	global_store_dwordx4 v110, v[120:123], s[36:37] nt
	v_cvt_pk_bf16_f32 v96, v67, v71
	v_cvt_pk_bf16_f32 v97, v75, v79
	v_cvt_pk_bf16_f32 v98, v83, v87
	v_cvt_pk_bf16_f32 v99, v91, v95
	global_store_dwordx4 v111, v[96:99], s[36:37] nt
	s_add_i32 s3, s3, 256
	s_min_u32 s12, s3, 0x324ff
	s_sub_u32 s12, s12, 0x24500
	s_lshr_b32 s13, s12, 10
	s_mul_i32 s13, s13, 37
	s_lshr_b32 s13, s13, 8
	s_mul_i32 s28, s13, 0x1c00
	s_sub_u32 s12, s12, s28
	s_and_b32 s28, s12, 31
	s_lshr_b32 s12, s12, 5
	s_mul_i32 s29, s13, 0x3800000
	s_lshl_b32 s32, s12, 18
	s_add_u32 s29, s29, s32
	s_lshl_b32 s32, s28, 8
	s_add_u32 s29, s29, s32
	s_add_u32 s8, s4, s29
	s_addc_u32 s9, s5, 0
	s_mul_i32 s29, s13, 0x1c00000
	s_mul_i32 s32, s28, 0xe0000
	s_add_u32 s29, s29, s32
	s_lshl_b32 s32, s12, 6
	s_add_u32 s29, s29, s32
	s_add_u32 s36, s6, s29
	s_addc_u32 s37, s7, 0
	s_nop 0
	global_load_dwordx4 v[64:67], v100, s[8:9] nt
	global_load_dwordx4 v[68:71], v101, s[8:9] nt
	global_load_dwordx4 v[72:75], v102, s[8:9] nt
	global_load_dwordx4 v[76:79], v103, s[8:9] nt
	global_load_dwordx4 v[80:83], v104, s[8:9] nt
	global_load_dwordx4 v[84:87], v105, s[8:9] nt
	global_load_dwordx4 v[88:91], v106, s[8:9] nt
	global_load_dwordx4 v[92:95], v107, s[8:9] nt
	s_waitcnt vmcnt(12)
	v_cvt_pk_bf16_f32 v112, v128, v132
	v_cvt_pk_bf16_f32 v113, v136, v140
	v_cvt_pk_bf16_f32 v114, v144, v148
	v_cvt_pk_bf16_f32 v115, v152, v156
	global_store_dwordx4 v108, v[112:115], s[10:11] nt
	v_cvt_pk_bf16_f32 v116, v129, v133
	v_cvt_pk_bf16_f32 v117, v137, v141
	v_cvt_pk_bf16_f32 v118, v145, v149
	v_cvt_pk_bf16_f32 v119, v153, v157
	global_store_dwordx4 v109, v[116:119], s[10:11] nt
	v_cvt_pk_bf16_f32 v120, v130, v134
	v_cvt_pk_bf16_f32 v121, v138, v142
	v_cvt_pk_bf16_f32 v122, v146, v150
	v_cvt_pk_bf16_f32 v123, v154, v158
	global_store_dwordx4 v110, v[120:123], s[10:11] nt
	v_cvt_pk_bf16_f32 v96, v131, v135
	v_cvt_pk_bf16_f32 v97, v139, v143
	v_cvt_pk_bf16_f32 v98, v147, v151
	v_cvt_pk_bf16_f32 v99, v155, v159
	global_store_dwordx4 v111, v[96:99], s[10:11] nt
	s_sub_i32 s33, s33, 1
	s_cmp_lg_u32 s33, 0
	s_cbranch_scc1 .Lcv0_loop
	s_waitcnt vmcnt(4)
	v_cvt_pk_bf16_f32 v112, v64, v68
	v_cvt_pk_bf16_f32 v113, v72, v76
	v_cvt_pk_bf16_f32 v114, v80, v84
	v_cvt_pk_bf16_f32 v115, v88, v92
	global_store_dwordx4 v108, v[112:115], s[36:37] nt
	v_cvt_pk_bf16_f32 v116, v65, v69
	v_cvt_pk_bf16_f32 v117, v73, v77
	v_cvt_pk_bf16_f32 v118, v81, v85
	v_cvt_pk_bf16_f32 v119, v89, v93
	global_store_dwordx4 v109, v[116:119], s[36:37] nt
	v_cvt_pk_bf16_f32 v120, v66, v70
	v_cvt_pk_bf16_f32 v121, v74, v78
	v_cvt_pk_bf16_f32 v122, v82, v86
	v_cvt_pk_bf16_f32 v123, v90, v94
	global_store_dwordx4 v110, v[120:123], s[36:37] nt
	v_cvt_pk_bf16_f32 v96, v67, v71
	v_cvt_pk_bf16_f32 v97, v75, v79
	v_cvt_pk_bf16_f32 v98, v83, v87
	v_cvt_pk_bf16_f32 v99, v91, v95
	global_store_dwordx4 v111, v[96:99], s[36:37] nt
	s_branch .LBB0_237

; __device__ __forceinline__ ConvTile conv_tile_desc(const unsigned long long* tab, int t) {
;     int si, di, N, K, nb, kb, e = 0, mode = 0, npad = 0;
;     if (t < CT_L0A) { si = 0; di = 10; N = L0C; K = DM; nb = t % 104; kb = t / 104; npad = 1; }
;     else if (t < CT_L0B) { const int u = t - CT_L0A; si = 1; di = 11; N = DM; K = DM; nb = u & 31; kb = u >> 5; }
;     else if (t < CT_L0C) { const int u = t - CT_L0B; si = 2; di = 12; N = FFN; K = DM; nb = u % 176; kb = u / 176; mode = 1; }
;     else if (t < CT_L0) { const int u = t - CT_L0C; si = 4; di = 13; N = DM; K = FFN; nb = u & 31; kb = u >> 5; }
;     else if (t < CT_A) { const int u = t - CT_L0; si = 5; di = 14; N = L1C; K = DM; nb = u % 100; kb = u / 100; npad = 1; }
;     else if (t < CT_B) { const int u = t - CT_A; si = 6; di = 15; N = DM; K = DM; nb = u & 31; kb = u >> 5; }
;     else if (t < CT_C) { const int u = t - CT_B; e = u / 14336; const int v = u % 14336; si = 7; di = 16; N = EXD; K = DM; nb = v % 224; kb = v / 224; mode = 1; }
;     else { const int u = (t < CT_TOTAL ? t : CT_TOTAL - 1) - CT_C; e = u / 7168; const int v = u % 7168; si = 9; di = 17; N = DM; K = EXD; nb = v & 31; kb = v >> 5; }
;     const int n0 = nb * 64;
;     int col0 = n0, nvalid = 64;
;     if (mode) { col0 = (n0 >> 8) * 128 + (n0 & 127); si += (n0 >> 7) & 1; }
;     if (npad) { nvalid = N - n0; if (nvalid <= 0) col0 = 0; }
;     ConvTile c;
;     const size_t KN = (size_t)K * N;
;     c.src = (const float*)tab[si] + (size_t)e * KN + (size_t)(kb * 32) * N + col0;
;     c.dst = (bf16_t*)tab[di] + (size_t)e * (mode ? 2 * KN : KN) + (size_t)n0 * K + kb * 32;
;     c.N = N; c.K = K; c.nvalid = nvalid;
;     return c;
; }
.LBB0_625:
	s_lshl_b32 s72, s33, 4
	s_lshl_b32 s33, s74, 6
	s_lshl_b32 s63, s74, 5
	s_and_b32 s63, s63, 0xffffff80
	s_and_b32 s75, s33, 64
	s_or_b32 s63, s63, s75
	s_bfe_u32 s78, s74, 0x10001
	s_and_b64 s[74:75], s[96:97], exec
	s_cselect_b32 s79, s33, s63
	s_cselect_b32 s63, 0, s78
	s_sub_i32 s33, s59, s33
	s_cmp_gt_i32 s33, 0
	s_cselect_b64 s[74:75], -1, 0
	s_lshl_b32 s64, s64, 3
	s_add_i32 s64, s64, 0
	s_lshl_b32 s63, s63, 3
	s_add_i32 s63, s64, s63
	s_add_i32 s63, s63, 0x20040
	v_mov_b32_e32 v58, s63
	ds_read_b64 v[58:59], v58
	s_mul_i32 s62, vcc_lo, s62
	s_mul_hi_u32 s63, s62, s59
	s_mul_i32 s62, s62, s59
	s_lshl_b64 s[62:63], s[62:63], 2
	s_waitcnt lgkmcnt(0)
	v_lshl_add_u64 v[58:59], v[58:59], 0, s[62:63]
	s_lshl_b32 s62, s65, 5
	s_mul_hi_i32 s63, s59, s62
	s_mul_i32 s62, s59, s62
	s_or_b64 s[74:75], s[60:61], s[74:75]
	s_lshl_b64 s[62:63], s[62:63], 2
	s_ashr_i32 s64, s79, 31
	v_lshl_add_u64 v[58:59], v[58:59], 0, s[62:63]
	s_and_b64 s[62:63], s[74:75], exec
	s_cselect_b32 s63, s64, 0
	s_cselect_b32 s62, s79, 0
	v_cmp_gt_i32_e32 vcc, s33, v136
	s_add_i32 s33, s59, s59
	s_lshl_b64 s[62:63], s[62:63], 2
	s_add_i32 s33, s33, s33
	v_lshl_add_u64 v[82:83], v[58:59], 0, s[62:63]
	v_mul_u32_u24_e32 v58, s59, v196
	v_mov_b32_e32 v74, s33
	v_lshlrev_b32_e32 v132, 2, v58
	s_or_b64 vcc, s[60:61], vcc
	v_mad_u32_u24 v76, s59, v196, v74
	v_lshl_add_u64 v[58:59], v[82:83], 0, v[132:133]
	v_cndmask_b32_e32 v60, 0, v136, vcc
	s_lshl_b32 s60, s59, 2
	s_mov_b32 s61, s73
	v_add_u32_e32 v84, s59, v76
	v_lshlrev_b32_e32 v132, 2, v60
	v_lshl_add_u64 v[66:67], v[58:59], 0, s[60:61]
	v_add_u32_e32 v86, s59, v84
	v_lshl_add_u64 v[62:63], v[66:67], 0, v[132:133]
	v_lshl_add_u64 v[66:67], v[66:67], 0, s[60:61]
	v_lshlrev_b32_e32 v74, 2, v76
	v_mov_b32_e32 v75, v133
	v_lshlrev_b32_e32 v76, 2, v84
	v_mov_b32_e32 v77, v133
	v_lshlrev_b32_e32 v84, 2, v86
	v_mov_b32_e32 v85, v133
	v_add_u32_e32 v86, s59, v86
	v_mov_b32_e32 v87, v133
	v_lshl_add_u64 v[68:69], v[66:67], 0, v[132:133]
	v_lshl_add_u64 v[66:67], v[66:67], 0, s[60:61]
	v_lshl_add_u64 v[74:75], v[82:83], 0, v[74:75]
	v_lshl_add_u64 v[76:77], v[82:83], 0, v[76:77]
	v_lshl_add_u64 v[84:85], v[82:83], 0, v[84:85]
	v_lshl_add_u64 v[82:83], v[86:87], 2, v[82:83]
	v_lshl_add_u64 v[60:61], v[58:59], 0, v[132:133]
	v_lshl_add_u64 v[70:71], v[66:67], 0, v[132:133]
	v_lshl_add_u64 v[74:75], v[74:75], 0, v[132:133]
	v_lshl_add_u64 v[78:79], v[76:77], 0, v[132:133]
	v_lshl_add_u64 v[84:85], v[84:85], 0, v[132:133]
	v_lshl_add_u64 v[86:87], v[82:83], 0, v[132:133]
	global_load_dwordx4 v[58:61], v[60:61], off nt
	s_nop 0
	global_load_dwordx4 v[62:65], v[62:63], off nt
	s_nop 0
	global_load_dwordx4 v[66:69], v[68:69], off nt
	s_nop 0
	global_load_dwordx4 v[70:73], v[70:71], off nt
	s_nop 0
	global_load_dwordx4 v[74:77], v[74:75], off nt
	s_nop 0
	global_load_dwordx4 v[78:81], v[78:79], off nt
	s_nop 0
	global_load_dwordx4 v[82:85], v[84:85], off nt
	s_nop 0
	global_load_dwordx4 v[86:89], v[86:87], off nt
	s_mov_b32 s59, s73
	s_movk_i32 s81, 0x100
	s_mov_b64 s[62:63], s[58:59]
	s_mov_b64 s[60:61], s[72:73]

; __device__ __forceinline__ ConvTile conv_tile_desc(const unsigned long long* tab, int t) {
;     ...
;     if (t < CT_L0A) { si = 0; di = 10; N = L0C; K = DM; nb = t % 104; kb = t / 104; npad = 1; }
;     else if (t < CT_L0B) { const int u = t - CT_L0A; si = 1; di = 11; N = DM; K = DM; nb = u & 31; kb = u >> 5; }
;     else if (t < CT_L0C) { const int u = t - CT_L0B; si = 2; di = 12; N = FFN; K = DM; nb = u % 176; kb = u / 176; mode = 1; }
;     else if (t < CT_L0) { const int u = t - CT_L0C; si = 4; di = 13; N = DM; K = FFN; nb = u & 31; kb = u >> 5; }
;     else if (t < CT_A) { const int u = t - CT_L0; si = 5; di = 14; N = L1C; K = DM; nb = u % 100; kb = u / 100; npad = 1; }
;     else if (t < CT_B) { const int u = t - CT_A; si = 6; di = 15; N = DM; K = DM; nb = u & 31; kb = u >> 5; }
;     else if (t < CT_C) { const int u = t - CT_B; e = u / 14336; const int v = u % 14336; si = 7; di = 16; N = EXD; K = DM; nb = v % 224; kb = v / 224; mode = 1; }
;     else { const int u = (t < CT_TOTAL ? t : CT_TOTAL - 1) - CT_C; e = u / 7168; const int v = u % 7168; si = 9; di = 17; N = DM; K = EXD; nb = v & 31; kb = v >> 5; }
;     const int n0 = nb * 64;
;     int col0 = n0, nvalid = 64;
;     if (mode) { col0 = (n0 >> 8) * 128 + (n0 & 127); si += (n0 >> 7) & 1; }
;     if (npad) { nvalid = N - n0; if (nvalid <= 0) col0 = 0; }
;     ConvTile c;
;     const size_t KN = (size_t)K * N;
;     c.src = (const float*)tab[si] + (size_t)e * KN + (size_t)(kb * 32) * N + col0;
;     c.dst = (bf16_t*)tab[di] + (size_t)e * (mode ? 2 * KN : KN) + (size_t)n0 * K + kb * 32;
;     c.N = N; c.K = K; c.nvalid = nvalid;
;     return c;
; }
.LBB0_656:
	s_lshl_b32 s62, s65, 6
	s_sub_i32 s61, s96, s62
	s_and_b64 s[58:59], s[58:59], exec
	s_cselect_b32 s63, 64, s61
	s_lshl_b32 s58, s75, 3
	s_add_i32 s58, s58, 0
	s_add_i32 s58, s58, 0x20040
	v_mov_b32_e32 v90, s58
	s_mul_i32 s72, s56, s96
	ds_read_b64 v[90:91], v90
	s_lshl_b64 s[58:59], s[72:73], s60
	s_lshl_b32 s60, s64, 5
	s_mul_i32 s59, s59, s74
	s_mul_hi_u32 s64, s58, s74
	s_add_i32 s59, s64, s59
	s_mul_i32 s58, s58, s74
	s_lshl_b64 s[58:59], s[58:59], 1
	s_waitcnt lgkmcnt(0)
	v_lshl_add_u64 v[90:91], v[90:91], 0, s[58:59]
	s_ashr_i32 s58, s62, 31
	s_mul_i32 s58, s56, s58
	s_mul_hi_u32 s59, s56, s62
	s_add_i32 s58, s59, s58
	s_mul_i32 s59, s57, s62
	s_add_i32 s59, s58, s59
	s_mul_i32 s58, s56, s62
	s_ashr_i32 s61, s60, 31
	s_lshl_b64 s[58:59], s[58:59], 1
	v_lshl_add_u64 v[90:91], v[90:91], 0, s[58:59]
	s_lshl_b64 s[58:59], s[60:61], 1
	v_mul_u32_u24_e32 v92, s56, v130
	v_lshl_add_u64 v[90:91], v[90:91], 0, s[58:59]
	v_lshlrev_b32_e32 v132, 1, v92
	v_lshl_add_u64 v[90:91], v[90:91], 0, v[132:133]
	v_lshlrev_b32_e32 v132, 1, v140
	v_cvt_pk_bf16_f32 v58, v58, v62
	v_cvt_pk_bf16_f32 v62, v66, v70
	v_cvt_pk_bf16_f32 v66, v74, v78
	v_cvt_pk_bf16_f32 v70, v82, v86
	v_cmp_gt_i32_e32 vcc, s63, v130
	v_lshl_add_u64 v[94:95], v[90:91], 0, v[132:133]
	s_lshl_b64 s[56:57], s[56:57], 1
	v_cndmask_b32_e32 v93, 0, v70, vcc
	v_cndmask_b32_e32 v92, 0, v66, vcc
	v_cndmask_b32_e32 v91, 0, v62, vcc
	v_cndmask_b32_e32 v90, 0, v58, vcc
	v_cvt_pk_bf16_f32 v58, v59, v63
	v_cvt_pk_bf16_f32 v59, v67, v71
	v_cvt_pk_bf16_f32 v62, v75, v79
	v_cvt_pk_bf16_f32 v63, v83, v87
	global_store_dwordx4 v[94:95], v[90:93], off nt
	v_cvt_pk_bf16_f32 v60, v60, v64
	v_cvt_pk_bf16_f32 v64, v84, v88
	v_cndmask_b32_e32 v93, 0, v63, vcc
	v_cndmask_b32_e32 v92, 0, v62, vcc
	v_cndmask_b32_e32 v91, 0, v59, vcc
	v_cndmask_b32_e32 v90, 0, v58, vcc
	v_lshl_add_u64 v[58:59], v[94:95], 0, s[56:57]
	v_cvt_pk_bf16_f32 v62, v68, v72
	v_cvt_pk_bf16_f32 v63, v76, v80
	s_add_i32 s65, s80, s33
	global_store_dwordx4 v[58:59], v[90:93], off nt
	s_min_i32 s72, s65, 0x324ff
	s_cmpk_gt_i32 s65, 0x19ff
	v_cndmask_b32_e32 v93, 0, v64, vcc
	v_cndmask_b32_e32 v92, 0, v63, vcc
	v_cndmask_b32_e32 v91, 0, v62, vcc
	v_cndmask_b32_e32 v90, 0, v60, vcc
	v_lshl_add_u64 v[62:63], v[58:59], 0, s[56:57]
	v_cvt_pk_bf16_f32 v58, v61, v65
	v_cvt_pk_bf16_f32 v59, v69, v73
	v_cvt_pk_bf16_f32 v60, v77, v81
	v_cvt_pk_bf16_f32 v61, v85, v89
	global_store_dwordx4 v[62:63], v[90:93], off nt
	v_cndmask_b32_e32 v61, 0, v61, vcc
	v_cndmask_b32_e32 v60, 0, v60, vcc
	v_cndmask_b32_e32 v59, 0, v59, vcc
	v_cndmask_b32_e32 v58, 0, v58, vcc
	v_lshl_add_u64 v[62:63], v[62:63], 0, s[56:57]
	s_mov_b64 s[96:97], -1
	global_store_dwordx4 v[62:63], v[58:61], off nt
	s_cbranch_scc0 .LBB0_681
	s_cmpk_gt_u32 s65, 0x21ff
	s_cbranch_scc0 .LBB0_678
	s_cmpk_gt_u32 s65, 0x4dff
	s_cbranch_scc0 .LBB0_675
	s_cmpk_gt_u32 s65, 0x63ff
	s_cbranch_scc0 .LBB0_672
	s_mov_b64 s[58:59], -1
	s_cmpk_gt_u32 s65, 0x7cff
	s_cbranch_scc0 .LBB0_669
	s_cmpk_gt_u32 s65, 0x84ff
	s_cbranch_scc0 .LBB0_666
	s_mov_b64 s[60:61], -1
	s_cmp_gt_u32 s65, 0x244ff
	s_mov_b64 s[56:57], -1
	s_cbranch_scc0 .LBB0_664
	s_add_i32 s56, s72, 0xbb00
	s_bfe_u32 s57, s56, 0x6000a
	s_mulk_i32 s57, 0x2493
	s_lshr_b32 s64, s57, 16
	s_mul_i32 s57, s64, 0x1c00
	s_sub_i32 s56, s56, s57
	s_and_b32 s75, s56, 31
	s_bfe_u32 s74, s56, 0xb0005
	s_mov_b64 s[56:57], 0

; __device__ __forceinline__ ConvTile conv_tile_desc(const unsigned long long* tab, int t) {
;     int si, di, N, K, nb, kb, e = 0, mode = 0, npad = 0;
;     if (t < CT_L0A) { si = 0; di = 10; N = L0C; K = DM; nb = t % 104; kb = t / 104; npad = 1; }
;     else if (t < CT_L0B) { const int u = t - CT_L0A; si = 1; di = 11; N = DM; K = DM; nb = u & 31; kb = u >> 5; }
;     else if (t < CT_L0C) { const int u = t - CT_L0B; si = 2; di = 12; N = FFN; K = DM; nb = u % 176; kb = u / 176; mode = 1; }
;     else if (t < CT_L0) { const int u = t - CT_L0C; si = 4; di = 13; N = DM; K = FFN; nb = u & 31; kb = u >> 5; }
;     else if (t < CT_A) { const int u = t - CT_L0; si = 5; di = 14; N = L1C; K = DM; nb = u % 100; kb = u / 100; npad = 1; }
;     else if (t < CT_B) { const int u = t - CT_A; si = 6; di = 15; N = DM; K = DM; nb = u & 31; kb = u >> 5; }
;     else if (t < CT_C) { const int u = t - CT_B; e = u / 14336; const int v = u % 14336; si = 7; di = 16; N = EXD; K = DM; nb = v % 224; kb = v / 224; mode = 1; }
;     else { const int u = (t < CT_TOTAL ? t : CT_TOTAL - 1) - CT_C; e = u / 7168; const int v = u % 7168; si = 9; di = 17; N = DM; K = EXD; nb = v & 31; kb = v >> 5; }
;     const int n0 = nb * 64;
;     int col0 = n0, nvalid = 64;
;     if (mode) { col0 = (n0 >> 8) * 128 + (n0 & 127); si += (n0 >> 7) & 1; }
;     if (npad) { nvalid = N - n0; if (nvalid <= 0) col0 = 0; }
;     ConvTile c;
;     const size_t KN = (size_t)K * N;
;     c.src = (const float*)tab[si] + (size_t)e * KN + (size_t)(kb * 32) * N + col0;
;     c.dst = (bf16_t*)tab[di] + (size_t)e * (mode ? 2 * KN : KN) + (size_t)n0 * K + kb * 32;
;     c.N = N; c.K = K; c.nvalid = nvalid;
;     return c;
; }
.LBB0_683:
	s_lshl_b32 s63, s75, 6
	s_lshl_b32 s65, s75, 5
	s_and_b32 s65, s65, 0xffffff80
	s_and_b32 s72, s63, 64
	s_or_b32 s65, s65, s72
	s_bfe_u32 s72, s75, 0x10001
	s_and_b64 s[60:61], s[60:61], exec
	s_cselect_b32 s65, s63, s65
	s_cselect_b32 s72, 0, s72
	s_sub_i32 s63, s56, s63
	s_cmp_gt_i32 s63, 0
	s_cselect_b64 s[60:61], -1, 0
	s_or_b64 s[60:61], s[58:59], s[60:61]
	s_and_b64 s[58:59], s[58:59], exec
	s_cselect_b32 s63, 64, s63
	s_lshl_b32 s57, s57, 3
	s_add_i32 s57, s57, 0
	s_lshl_b32 s58, s72, 3
	s_add_i32 s57, s57, s58
	s_add_i32 s57, s57, 0x20040
	v_mov_b32_e32 v58, s57
	ds_read_b64 v[58:59], v58
	s_mul_i32 s57, s62, s64
	s_mul_hi_u32 s59, s57, s56
	s_mul_i32 s58, s57, s56
	s_lshl_b64 s[58:59], s[58:59], 2
	s_lshl_b32 s57, s74, 5
	s_waitcnt lgkmcnt(0)
	v_lshl_add_u64 v[58:59], v[58:59], 0, s[58:59]
	s_ashr_i32 s58, s57, 31
	s_mul_i32 s58, s56, s58
	s_mul_hi_u32 s59, s56, s57
	s_add_i32 s59, s59, s58
	s_mul_i32 s58, s56, s57
	s_lshl_b64 s[58:59], s[58:59], 2
	s_ashr_i32 s57, s65, 31
	v_lshl_add_u64 v[58:59], v[58:59], 0, s[58:59]
	s_and_b64 s[58:59], s[60:61], exec
	s_cselect_b32 s59, s57, 0
	s_cselect_b32 s58, s65, 0
	s_lshl_b64 s[58:59], s[58:59], 2
	s_ashr_i32 s57, s56, 31
	v_lshl_add_u64 v[82:83], v[58:59], 0, s[58:59]
	s_lshl_b64 s[58:59], s[56:57], 2
	s_add_i32 s57, s56, s56
	v_mul_u32_u24_e32 v58, s56, v140
	v_cmp_gt_i32_e32 vcc, s63, v130
	s_add_i32 s57, s57, s56
	v_lshlrev_b32_e32 v132, 2, v58
	v_cndmask_b32_e32 v60, 0, v130, vcc
	v_mov_b32_e32 v74, s57
	v_lshl_add_u64 v[58:59], v[82:83], 0, v[132:133]
	v_lshlrev_b32_e32 v132, 2, v60
	v_mul_u32_u24_e32 v60, s56, v199
	v_mad_u32_u24 v74, s56, v199, v74
	v_lshlrev_b32_e32 v60, 2, v60
	v_mov_b32_e32 v61, v133
	v_mov_b32_e32 v75, v133
	v_add_u32_e32 v84, s56, v74
	v_mov_b32_e32 v85, v133
	v_lshl_add_u64 v[66:67], v[82:83], 0, v[60:61]
	v_lshl_add_u64 v[76:77], v[74:75], 2, v[82:83]
	v_lshl_add_u64 v[74:75], v[84:85], 2, v[82:83]
	v_add_u32_e32 v84, s56, v84
	v_lshl_add_u64 v[62:63], v[66:67], 0, v[132:133]
	v_lshl_add_u64 v[66:67], v[66:67], 0, s[58:59]
	v_lshl_add_u64 v[86:87], v[84:85], 2, v[82:83]
	v_add_u32_e32 v84, s56, v84
	v_lshl_add_u64 v[68:69], v[66:67], 0, v[132:133]
	v_lshl_add_u64 v[66:67], v[66:67], 0, s[58:59]
	v_lshl_add_u64 v[82:83], v[84:85], 2, v[82:83]
	v_lshl_add_u64 v[58:59], v[58:59], 0, v[132:133]
	v_lshl_add_u64 v[70:71], v[66:67], 0, v[132:133]
	v_lshl_add_u64 v[76:77], v[76:77], 0, v[132:133]
	v_lshl_add_u64 v[78:79], v[74:75], 0, v[132:133]
	v_lshl_add_u64 v[86:87], v[86:87], 0, v[132:133]
	v_lshl_add_u64 v[88:89], v[82:83], 0, v[132:133]
	global_load_dwordx4 v[58:61], v[58:59], off nt
	s_nop 0
	global_load_dwordx4 v[62:65], v[62:63], off nt
	s_nop 0
	global_load_dwordx4 v[66:69], v[68:69], off nt
	s_nop 0
	global_load_dwordx4 v[70:73], v[70:71], off nt
	s_nop 0
	global_load_dwordx4 v[74:77], v[76:77], off nt
	s_nop 0
	global_load_dwordx4 v[78:81], v[78:79], off nt
	s_nop 0
	global_load_dwordx4 v[82:85], v[86:87], off nt
	s_nop 0
	global_load_dwordx4 v[86:89], v[88:89], off nt
	s_mov_b64 s[96:97], s[76:77]
	s_branch .LBB0_685

; __device__ __forceinline__ ConvTile conv_tile_desc(const unsigned long long* tab, int t) {
;     ...
;     if (t < CT_L0A) { si = 0; di = 10; N = L0C; K = DM; nb = t % 104; kb = t / 104; npad = 1; }
;     else if (t < CT_L0B) { const int u = t - CT_L0A; si = 1; di = 11; N = DM; K = DM; nb = u & 31; kb = u >> 5; }
;     else if (t < CT_L0C) { const int u = t - CT_L0B; si = 2; di = 12; N = FFN; K = DM; nb = u % 176; kb = u / 176; mode = 1; }
;     else if (t < CT_L0) { const int u = t - CT_L0C; si = 4; di = 13; N = DM; K = FFN; nb = u & 31; kb = u >> 5; }
;     else if (t < CT_A) { const int u = t - CT_L0; si = 5; di = 14; N = L1C; K = DM; nb = u % 100; kb = u / 100; npad = 1; }
;     else if (t < CT_B) { const int u = t - CT_A; si = 6; di = 15; N = DM; K = DM; nb = u & 31; kb = u >> 5; }
;     else if (t < CT_C) { const int u = t - CT_B; e = u / 14336; const int v = u % 14336; si = 7; di = 16; N = EXD; K = DM; nb = v % 224; kb = v / 224; mode = 1; }
;     else { const int u = (t < CT_TOTAL ? t : CT_TOTAL - 1) - CT_C; e = u / 7168; const int v = u % 7168; si = 9; di = 17; N = DM; K = EXD; nb = v & 31; kb = v >> 5; }
;     const int n0 = nb * 64;
;     int col0 = n0, nvalid = 64;
;     if (mode) { col0 = (n0 >> 8) * 128 + (n0 & 127); si += (n0 >> 7) & 1; }
;     if (npad) { nvalid = N - n0; if (nvalid <= 0) col0 = 0; }
;     ConvTile c;
;     const size_t KN = (size_t)K * N;
;     c.src = (const float*)tab[si] + (size_t)e * KN + (size_t)(kb * 32) * N + col0;
;     c.dst = (bf16_t*)tab[di] + (size_t)e * (mode ? 2 * KN : KN) + (size_t)n0 * K + kb * 32;
;     c.N = N; c.K = K; c.nvalid = nvalid;
;     return c;
; }
.LBB0_715:
	s_lshl_b32 s62, s65, 6
	s_sub_i32 s61, s96, s62
	s_and_b64 s[58:59], s[58:59], exec
	s_cselect_b32 s63, 64, s61
	s_lshl_b32 s58, s75, 3
	s_add_i32 s58, s58, 0
	s_add_i32 s58, s58, 0x20040
	v_mov_b32_e32 v90, s58
	s_mul_i32 s72, s56, s96
	ds_read_b64 v[90:91], v90
	s_lshl_b64 s[58:59], s[72:73], s60
	s_lshl_b32 s60, s64, 5
	s_mul_i32 s59, s59, s74
	s_mul_hi_u32 s64, s58, s74
	s_add_i32 s59, s64, s59
	s_mul_i32 s58, s58, s74
	s_lshl_b64 s[58:59], s[58:59], 1
	s_waitcnt lgkmcnt(0)
	v_lshl_add_u64 v[90:91], v[90:91], 0, s[58:59]
	s_ashr_i32 s58, s62, 31
	s_mul_i32 s58, s56, s58
	s_mul_hi_u32 s59, s56, s62
	s_add_i32 s58, s59, s58
	s_mul_i32 s59, s57, s62
	s_add_i32 s59, s58, s59
	s_mul_i32 s58, s56, s62
	s_ashr_i32 s61, s60, 31
	s_lshl_b64 s[58:59], s[58:59], 1
	v_lshl_add_u64 v[90:91], v[90:91], 0, s[58:59]
	s_lshl_b64 s[58:59], s[60:61], 1
	v_mul_u32_u24_e32 v92, s56, v130
	v_lshl_add_u64 v[90:91], v[90:91], 0, s[58:59]
	v_lshlrev_b32_e32 v132, 1, v92
	v_lshl_add_u64 v[90:91], v[90:91], 0, v[132:133]
	v_lshlrev_b32_e32 v132, 1, v140
	v_cvt_pk_bf16_f32 v58, v58, v62
	v_cvt_pk_bf16_f32 v62, v66, v70
	v_cvt_pk_bf16_f32 v66, v74, v78
	v_cvt_pk_bf16_f32 v70, v82, v86
	v_cmp_gt_i32_e32 vcc, s63, v130
	v_lshl_add_u64 v[94:95], v[90:91], 0, v[132:133]
	s_lshl_b64 s[56:57], s[56:57], 1
	v_cndmask_b32_e32 v93, 0, v70, vcc
	v_cndmask_b32_e32 v92, 0, v66, vcc
	v_cndmask_b32_e32 v91, 0, v62, vcc
	v_cndmask_b32_e32 v90, 0, v58, vcc
	v_cvt_pk_bf16_f32 v58, v59, v63
	v_cvt_pk_bf16_f32 v59, v67, v71
	v_cvt_pk_bf16_f32 v62, v75, v79
	v_cvt_pk_bf16_f32 v63, v83, v87
	global_store_dwordx4 v[94:95], v[90:93], off nt
	v_cvt_pk_bf16_f32 v60, v60, v64
	v_cvt_pk_bf16_f32 v64, v84, v88
	v_cndmask_b32_e32 v93, 0, v63, vcc
	v_cndmask_b32_e32 v92, 0, v62, vcc
	v_cndmask_b32_e32 v91, 0, v59, vcc
	v_cndmask_b32_e32 v90, 0, v58, vcc
	v_lshl_add_u64 v[58:59], v[94:95], 0, s[56:57]
	v_cvt_pk_bf16_f32 v62, v68, v72
	v_cvt_pk_bf16_f32 v63, v76, v80
	s_add_i32 s33, s88, s33
	global_store_dwordx4 v[58:59], v[90:93], off nt
	s_min_i32 s72, s33, 0x324ff
	s_cmpk_gt_i32 s33, 0x19ff
	v_cndmask_b32_e32 v93, 0, v64, vcc
	v_cndmask_b32_e32 v92, 0, v63, vcc
	v_cndmask_b32_e32 v91, 0, v62, vcc
	v_cndmask_b32_e32 v90, 0, v60, vcc
	v_lshl_add_u64 v[62:63], v[58:59], 0, s[56:57]
	v_cvt_pk_bf16_f32 v58, v61, v65
	v_cvt_pk_bf16_f32 v59, v69, v73
	v_cvt_pk_bf16_f32 v60, v77, v81
	v_cvt_pk_bf16_f32 v61, v85, v89
	global_store_dwordx4 v[62:63], v[90:93], off nt
	v_cndmask_b32_e32 v61, 0, v61, vcc
	v_cndmask_b32_e32 v60, 0, v60, vcc
	v_cndmask_b32_e32 v59, 0, v59, vcc
	v_cndmask_b32_e32 v58, 0, v58, vcc
	v_lshl_add_u64 v[62:63], v[62:63], 0, s[56:57]
	s_mov_b64 s[96:97], -1
	global_store_dwordx4 v[62:63], v[58:61], off nt
	s_cbranch_scc0 .LBB0_740
	s_cmpk_gt_u32 s33, 0x21ff
	s_cbranch_scc0 .LBB0_737
	s_cmpk_gt_u32 s33, 0x4dff
	s_cbranch_scc0 .LBB0_734
	s_cmpk_gt_u32 s33, 0x63ff
	s_cbranch_scc0 .LBB0_731
	s_mov_b64 s[58:59], -1
	s_cmpk_gt_u32 s33, 0x7cff
	s_cbranch_scc0 .LBB0_728
	s_cmpk_gt_u32 s33, 0x84ff
	s_cbranch_scc0 .LBB0_725
	s_mov_b64 s[60:61], -1
	s_cmp_gt_u32 s33, 0x244ff
	s_mov_b64 s[56:57], -1
	s_cbranch_scc0 .LBB0_723
	s_add_i32 s56, s72, 0xbb00
	s_bfe_u32 s57, s56, 0x6000a
	s_mulk_i32 s57, 0x2493
	s_lshr_b32 s64, s57, 16
	s_mul_i32 s57, s64, 0x1c00
	s_sub_i32 s56, s56, s57
	s_and_b32 s75, s56, 31
	s_bfe_u32 s74, s56, 0xb0005
	s_mov_b64 s[56:57], 0

;     __device__ bool next(int i, Unit& u) const {
;         const long L = (long)i * G + c; if (L >= nwg) return false;
;         int wgid = (int)L; { const int q = nwg / NXCD, r = nwg % NXCD, xcd = wgid % NXCD, off = wgid / NXCD; wgid = (xcd < r ? xcd * (q + 1) : r * (q + 1) + (xcd - r) * q) + off; }
;         const int nig = WGM * nN, gid = wgid / nig, fm = gid * WGM, gsz = (nM - fm) < WGM ? (nM - fm) : WGM;
;         u.pm = fm + ((wgid % nig) % gsz); u.pn = (wgid % nig) / gsz; u.k0 = 0; return true;
;     }
.LBB0_1335:
	s_or_b64 exec, exec, s[0:1]
	s_cmpk_lt_i32 s90, 0xd8
	s_cselect_b64 s[0:1], -1, 0
	v_mov_b32_e32 v14, v0
	s_waitcnt lgkmcnt(0)
	s_barrier
	s_and_b64 vcc, exec, s[0:1]
	v_readfirstlane_b32 s14, v14
	s_cbranch_vccz .LBB0_1337
	s_add_i32 s2, s90, s85
	s_and_b32 s3, s2, -8
	s_sub_i32 s3, s90, s3
	s_mul_i32 s5, s3, 0x6a
	s_add_i32 s5, s5, 2
	s_ashr_i32 s2, s2, 3
	s_mul_i32 s4, s3, 0x6b
	s_cmp_lt_i32 s3, 2
	s_cselect_b32 s3, s4, s5
	s_add_i32 s3, s3, s2
	s_mul_hi_i32 s2, s3, 0x51eb851f
	s_lshr_b32 s4, s2, 31
	s_ashr_i32 s2, s2, 6
	s_add_i32 s2, s2, s4
	s_lshl_b32 s4, s2, 3
	s_sub_i32 s5, 34, s4
	s_mulk_i32 s2, 0xc8
	s_min_u32 s5, s5, 8
	s_sub_i32 s7, s3, s2
	s_sext_i32_i16 s2, s7
	v_cvt_f32_ubyte0_e32 v3, s5
	v_cvt_f32_i32_e32 v2, s2
	v_rcp_iflag_f32_e32 v4, v3
	s_ashr_i32 s2, s2, 30
	s_or_b32 s6, s2, 1
	v_mul_f32_e32 v4, v2, v4
	v_trunc_f32_e32 v4, v4
	v_fma_f32 v2, -v4, v3, v2
	v_cvt_i32_f32_e32 v4, v4
	v_cmp_ge_f32_e64 s[2:3], |v2|, v3
	s_and_b64 s[2:3], s[2:3], exec
	s_cselect_b32 s2, s6, 0
	v_readfirstlane_b32 s3, v4
	s_add_i32 s2, s3, s2
	s_sext_i32_i16 s6, s2
	s_mul_i32 s2, s2, s5
	s_sub_i32 s2, s7, s2
	s_sext_i32_i16 s2, s2
	s_add_i32 s16, s4, s2

;     __device__ bool next(int i, Unit& u) const {
;         const long L = (long)i * G + c; if (L >= nwg) return false;
;         int wgid = (int)L; { const int q = nwg / NXCD, r = nwg % NXCD, xcd = wgid % NXCD, off = wgid / NXCD; wgid = (xcd < r ? xcd * (q + 1) : r * (q + 1) + (xcd - r) * q) + off; }
;         const int nig = WGM * nN, gid = wgid / nig, fm = gid * WGM, gsz = (nM - fm) < WGM ? (nM - fm) : WGM;
;         u.pm = fm + ((wgid % nig) % gsz); u.pn = (wgid % nig) / gsz; u.k0 = 0; return true;
; template <class Epi, class Sched, bool ALIGN_EPI = false, bool SP2 = false>
; __device__ __forceinline__ void gemm_phase(PG8_LAS unsigned char* lds, const Gemm g, const Sched& S, const Epi& E) {
;     ...
;         const bool has_next = S.next(ui + 1, nxt);
.LBB0_1343:
	s_add_i32 s33, s33, 1
	s_mul_i32 s0, s33, s97
	s_mul_hi_u32 s1, s33, 0xd8
	s_add_i32 s1, s1, s0
	s_mul_i32 s0, s33, 0xd8
	s_add_u32 s22, s0, s90
	s_addc_u32 s23, s1, s91
	v_cmp_gt_i64_e32 vcc, s[22:23], v[146:147]
	v_cmp_lt_i64_e64 s[0:1], s[22:23], v[144:145]
	s_cbranch_vccnz .LBB0_1349
	s_ashr_i32 s7, s22, 31
	s_lshr_b32 s7, s7, 29
	s_add_i32 s7, s22, s7
	s_and_b32 s18, s7, -8
	s_sub_i32 s20, s22, s18
	s_cmp_gt_i32 s20, 1
	s_mov_b64 s[18:19], -1
	s_cbranch_scc0 .LBB0_1346
	s_mul_i32 s18, s20, 0x6a
	s_add_i32 s21, s18, 2
	s_mov_b64 s[18:19], 0

; __device__ __forceinline__ ConvTile conv_tile_desc(const unsigned long long* tab, int t) {
;     ...
;     else { const int u = (t < CT_TOTAL ? t : CT_TOTAL - 1) - CT_C; e = u / 7168; const int v = u % 7168; si = 9; di = 17; N = DM; K = EXD; nb = v & 31; kb = v >> 5; }
;     const int n0 = nb * 64;
;     int col0 = n0, nvalid = 64;
;     if (mode) { col0 = (n0 >> 8) * 128 + (n0 & 127); si += (n0 >> 7) & 1; }
;     if (npad) { nvalid = N - n0; if (nvalid <= 0) col0 = 0; }
;     ConvTile c;
;     const size_t KN = (size_t)K * N;
;     c.src = (const float*)tab[si] + (size_t)e * KN + (size_t)(kb * 32) * N + col0;
;     c.dst = (bf16_t*)tab[di] + (size_t)e * (mode ? 2 * KN : KN) + (size_t)n0 * K + kb * 32;
;     c.N = N; c.K = K; c.nvalid = nvalid;
;     return c;
; }
.Lcv1_start:
	v_and_b32_e32 v96, 63, v0
	v_lshrrev_b32_e32 v97, 6, v0
	v_lshrrev_b32_e32 v98, 4, v96
	v_and_b32_e32 v99, 15, v96
	v_readfirstlane_b32 s2, v97
	v_lshlrev_b32_e32 v100, 16, v98
	v_lshl_add_u32 v100, v99, 4, v100
	v_add_u32_e32 v101, 0x2000, v100
	v_add_u32_e32 v102, 0x4000, v100
	v_add_u32_e32 v103, 0x6000, v100
	v_add_u32_e32 v104, 0x8000, v100
	v_add_u32_e32 v105, 0xa000, v100
	v_add_u32_e32 v106, 0xc000, v100
	v_add_u32_e32 v107, 0xe000, v100
	v_mul_u32_u24_e32 v108, 0xe000, v99
	v_lshl_add_u32 v108, v98, 4, v108
	v_add_u32_e32 v109, 0x3800, v108
	v_add_u32_e32 v110, 0x7000, v108
	v_add_u32_e32 v111, 0xa800, v108
	v_mov_b32_e32 v112, 0x20088
	v_mov_b32_e32 v113, 0x200c8
	ds_read_b64 v[114:115], v112
	ds_read_b64 v[116:117], v113
	s_waitcnt lgkmcnt(0)
	v_readfirstlane_b32 s4, v114
	v_readfirstlane_b32 s5, v115
	v_readfirstlane_b32 s6, v116
	v_readfirstlane_b32 s7, v117
	s_sub_i32 s3, s90, 216
	s_lshl_b32 s3, s3, 3
	s_add_i32 s3, s3, s2
	s_add_i32 s3, s3, 0x2e400
	s_nop 4
	s_min_u32 s12, s3, 0x324ff
	s_sub_u32 s12, s12, 0x24500
	s_lshr_b32 s13, s12, 10
	s_mul_i32 s13, s13, 37
	s_lshr_b32 s13, s13, 8
	s_mul_i32 s28, s13, 0x1c00
	s_sub_u32 s12, s12, s28
	s_and_b32 s28, s12, 31
	s_lshr_b32 s12, s12, 5
	s_mul_i32 s29, s13, 0x3800000
	s_lshl_b32 s32, s12, 18
	s_add_u32 s29, s29, s32
	s_lshl_b32 s32, s28, 8
	s_add_u32 s29, s29, s32
	s_add_u32 s8, s4, s29
	s_addc_u32 s9, s5, 0
	s_mul_i32 s29, s13, 0x1c00000
	s_mul_i32 s32, s28, 0xe0000
	s_add_u32 s29, s29, s32
	s_lshl_b32 s32, s12, 6
	s_add_u32 s29, s29, s32
	s_add_u32 s10, s6, s29
	s_addc_u32 s11, s7, 0
	s_nop 0
	global_load_dwordx4 v[128:131], v100, s[8:9] nt
	global_load_dwordx4 v[132:135], v101, s[8:9] nt
	global_load_dwordx4 v[136:139], v102, s[8:9] nt
	global_load_dwordx4 v[140:143], v103, s[8:9] nt
	global_load_dwordx4 v[144:147], v104, s[8:9] nt
	global_load_dwordx4 v[148:151], v105, s[8:9] nt
	global_load_dwordx4 v[152:155], v106, s[8:9] nt
	global_load_dwordx4 v[156:159], v107, s[8:9] nt
	s_add_i32 s3, s3, 320
	s_min_u32 s12, s3, 0x324ff
	s_sub_u32 s12, s12, 0x24500
	s_lshr_b32 s13, s12, 10
	s_mul_i32 s13, s13, 37
	s_lshr_b32 s13, s13, 8
	s_mul_i32 s28, s13, 0x1c00
	s_sub_u32 s12, s12, s28
	s_and_b32 s28, s12, 31
	s_lshr_b32 s12, s12, 5
	s_mul_i32 s29, s13, 0x3800000
	s_lshl_b32 s32, s12, 18
	s_add_u32 s29, s29, s32
	s_lshl_b32 s32, s28, 8
	s_add_u32 s29, s29, s32
	s_add_u32 s8, s4, s29
	s_addc_u32 s9, s5, 0
	s_mul_i32 s29, s13, 0x1c00000
	s_mul_i32 s32, s28, 0xe0000
	s_add_u32 s29, s29, s32
	s_lshl_b32 s32, s12, 6
	s_add_u32 s29, s29, s32
	s_add_u32 s36, s6, s29
	s_addc_u32 s37, s7, 0
	s_nop 0
	global_load_dwordx4 v[64:67], v100, s[8:9] nt
	global_load_dwordx4 v[68:71], v101, s[8:9] nt
	global_load_dwordx4 v[72:75], v102, s[8:9] nt
	global_load_dwordx4 v[76:79], v103, s[8:9] nt
	global_load_dwordx4 v[80:83], v104, s[8:9] nt
	global_load_dwordx4 v[84:87], v105, s[8:9] nt
	global_load_dwordx4 v[88:91], v106, s[8:9] nt
	global_load_dwordx4 v[92:95], v107, s[8:9] nt
	s_waitcnt vmcnt(8)
	v_cvt_pk_bf16_f32 v112, v128, v132
	v_cvt_pk_bf16_f32 v113, v136, v140
	v_cvt_pk_bf16_f32 v114, v144, v148
	v_cvt_pk_bf16_f32 v115, v152, v156
	global_store_dwordx4 v108, v[112:115], s[10:11] nt
	v_cvt_pk_bf16_f32 v116, v129, v133
	v_cvt_pk_bf16_f32 v117, v137, v141
	v_cvt_pk_bf16_f32 v118, v145, v149
	v_cvt_pk_bf16_f32 v119, v153, v157
	global_store_dwordx4 v109, v[116:119], s[10:11] nt
	v_cvt_pk_bf16_f32 v120, v130, v134
	v_cvt_pk_bf16_f32 v121, v138, v142
	v_cvt_pk_bf16_f32 v122, v146, v150
	v_cvt_pk_bf16_f32 v123, v154, v158
	global_store_dwordx4 v110, v[120:123], s[10:11] nt
	v_cvt_pk_bf16_f32 v96, v131, v135
	v_cvt_pk_bf16_f32 v97, v139, v143
	v_cvt_pk_bf16_f32 v98, v147, v151
	v_cvt_pk_bf16_f32 v99, v155, v159
	global_store_dwordx4 v111, v[96:99], s[10:11] nt
	s_movk_i32 s33, 25
; __device__ __forceinline__ ConvTile conv_tile_desc(const unsigned long long* tab, int t) {
;     ...
;     else { const int u = (t < CT_TOTAL ? t : CT_TOTAL - 1) - CT_C; e = u / 7168; const int v = u % 7168; si = 9; di = 17; N = DM; K = EXD; nb = v & 31; kb = v >> 5; }
;     const int n0 = nb * 64;
;     int col0 = n0, nvalid = 64;
;     if (mode) { col0 = (n0 >> 8) * 128 + (n0 & 127); si += (n0 >> 7) & 1; }
;     if (npad) { nvalid = N - n0; if (nvalid <= 0) col0 = 0; }
;     ConvTile c;
;     const size_t KN = (size_t)K * N;
;     c.src = (const float*)tab[si] + (size_t)e * KN + (size_t)(kb * 32) * N + col0;
;     c.dst = (bf16_t*)tab[di] + (size_t)e * (mode ? 2 * KN : KN) + (size_t)n0 * K + kb * 32;
;     c.N = N; c.K = K; c.nvalid = nvalid;
;     return c;
; }
.Lcv1_loop:
	s_add_i32 s3, s3, 320
	s_min_u32 s12, s3, 0x324ff
	s_sub_u32 s12, s12, 0x24500
	s_lshr_b32 s13, s12, 10
	s_mul_i32 s13, s13, 37
	s_lshr_b32 s13, s13, 8
	s_mul_i32 s28, s13, 0x1c00
	s_sub_u32 s12, s12, s28
	s_and_b32 s28, s12, 31
	s_lshr_b32 s12, s12, 5
	s_mul_i32 s29, s13, 0x3800000
	s_lshl_b32 s32, s12, 18
	s_add_u32 s29, s29, s32
	s_lshl_b32 s32, s28, 8
	s_add_u32 s29, s29, s32
	s_add_u32 s8, s4, s29
	s_addc_u32 s9, s5, 0
	s_mul_i32 s29, s13, 0x1c00000
	s_mul_i32 s32, s28, 0xe0000
	s_add_u32 s29, s29, s32
	s_lshl_b32 s32, s12, 6
	s_add_u32 s29, s29, s32
	s_add_u32 s10, s6, s29
	s_addc_u32 s11, s7, 0
	s_nop 0
	global_load_dwordx4 v[128:131], v100, s[8:9] nt
	global_load_dwordx4 v[132:135], v101, s[8:9] nt
	global_load_dwordx4 v[136:139], v102, s[8:9] nt
	global_load_dwordx4 v[140:143], v103, s[8:9] nt
	global_load_dwordx4 v[144:147], v104, s[8:9] nt
	global_load_dwordx4 v[148:151], v105, s[8:9] nt
	global_load_dwordx4 v[152:155], v106, s[8:9] nt
	global_load_dwordx4 v[156:159], v107, s[8:9] nt
	s_waitcnt vmcnt(12)
	v_cvt_pk_bf16_f32 v112, v64, v68
	v_cvt_pk_bf16_f32 v113, v72, v76
	v_cvt_pk_bf16_f32 v114, v80, v84
	v_cvt_pk_bf16_f32 v115, v88, v92
	global_store_dwordx4 v108, v[112:115], s[36:37] nt
	v_cvt_pk_bf16_f32 v116, v65, v69
	v_cvt_pk_bf16_f32 v117, v73, v77
	v_cvt_pk_bf16_f32 v118, v81, v85
	v_cvt_pk_bf16_f32 v119, v89, v93
	global_store_dwordx4 v109, v[116:119], s[36:37] nt
	v_cvt_pk_bf16_f32 v120, v66, v70
	v_cvt_pk_bf16_f32 v121, v74, v78
	v_cvt_pk_bf16_f32 v122, v82, v86
	v_cvt_pk_bf16_f32 v123, v90, v94
	global_store_dwordx4 v110, v[120:123], s[36:37] nt
	v_cvt_pk_bf16_f32 v96, v67, v71
	v_cvt_pk_bf16_f32 v97, v75, v79
	v_cvt_pk_bf16_f32 v98, v83, v87
	v_cvt_pk_bf16_f32 v99, v91, v95
	global_store_dwordx4 v111, v[96:99], s[36:37] nt
	s_add_i32 s3, s3, 320
	s_min_u32 s12, s3, 0x324ff
	s_sub_u32 s12, s12, 0x24500
	s_lshr_b32 s13, s12, 10
	s_mul_i32 s13, s13, 37
	s_lshr_b32 s13, s13, 8
	s_mul_i32 s28, s13, 0x1c00
	s_sub_u32 s12, s12, s28
	s_and_b32 s28, s12, 31
	s_lshr_b32 s12, s12, 5
	s_mul_i32 s29, s13, 0x3800000
	s_lshl_b32 s32, s12, 18
	s_add_u32 s29, s29, s32
	s_lshl_b32 s32, s28, 8
	s_add_u32 s29, s29, s32
	s_add_u32 s8, s4, s29
	s_addc_u32 s9, s5, 0
	s_mul_i32 s29, s13, 0x1c00000
	s_mul_i32 s32, s28, 0xe0000
	s_add_u32 s29, s29, s32
	s_lshl_b32 s32, s12, 6
	s_add_u32 s29, s29, s32
	s_add_u32 s36, s6, s29
	s_addc_u32 s37, s7, 0
	s_nop 0
	global_load_dwordx4 v[64:67], v100, s[8:9] nt
	global_load_dwordx4 v[68:71], v101, s[8:9] nt
	global_load_dwordx4 v[72:75], v102, s[8:9] nt
	global_load_dwordx4 v[76:79], v103, s[8:9] nt
	global_load_dwordx4 v[80:83], v104, s[8:9] nt
	global_load_dwordx4 v[84:87], v105, s[8:9] nt
	global_load_dwordx4 v[88:91], v106, s[8:9] nt
	global_load_dwordx4 v[92:95], v107, s[8:9] nt
	s_waitcnt vmcnt(12)
	v_cvt_pk_bf16_f32 v112, v128, v132
	v_cvt_pk_bf16_f32 v113, v136, v140
	v_cvt_pk_bf16_f32 v114, v144, v148
	v_cvt_pk_bf16_f32 v115, v152, v156
	global_store_dwordx4 v108, v[112:115], s[10:11] nt
	v_cvt_pk_bf16_f32 v116, v129, v133
	v_cvt_pk_bf16_f32 v117, v137, v141
	v_cvt_pk_bf16_f32 v118, v145, v149
	v_cvt_pk_bf16_f32 v119, v153, v157
	global_store_dwordx4 v109, v[116:119], s[10:11] nt
	v_cvt_pk_bf16_f32 v120, v130, v134
	v_cvt_pk_bf16_f32 v121, v138, v142
	v_cvt_pk_bf16_f32 v122, v146, v150
	v_cvt_pk_bf16_f32 v123, v154, v158
	global_store_dwordx4 v110, v[120:123], s[10:11] nt
	v_cvt_pk_bf16_f32 v96, v131, v135
	v_cvt_pk_bf16_f32 v97, v139, v143
	v_cvt_pk_bf16_f32 v98, v147, v151
	v_cvt_pk_bf16_f32 v99, v155, v159
	global_store_dwordx4 v111, v[96:99], s[10:11] nt
	s_sub_i32 s33, s33, 1
	s_cmp_lg_u32 s33, 0
	s_cbranch_scc1 .Lcv1_loop
	s_waitcnt vmcnt(4)
	v_cvt_pk_bf16_f32 v112, v64, v68
	v_cvt_pk_bf16_f32 v113, v72, v76
	v_cvt_pk_bf16_f32 v114, v80, v84
	v_cvt_pk_bf16_f32 v115, v88, v92
	global_store_dwordx4 v108, v[112:115], s[36:37] nt
	v_cvt_pk_bf16_f32 v116, v65, v69
	v_cvt_pk_bf16_f32 v117, v73, v77
	v_cvt_pk_bf16_f32 v118, v81, v85
	v_cvt_pk_bf16_f32 v119, v89, v93
	global_store_dwordx4 v109, v[116:119], s[36:37] nt
	v_cvt_pk_bf16_f32 v120, v66, v70
	v_cvt_pk_bf16_f32 v121, v74, v78
	v_cvt_pk_bf16_f32 v122, v82, v86
	v_cvt_pk_bf16_f32 v123, v90, v94
	global_store_dwordx4 v110, v[120:123], s[36:37] nt
	v_cvt_pk_bf16_f32 v96, v67, v71
	v_cvt_pk_bf16_f32 v97, v75, v79
	v_cvt_pk_bf16_f32 v98, v83, v87
	v_cvt_pk_bf16_f32 v99, v91, v95
	global_store_dwordx4 v111, v[96:99], s[36:37] nt
	s_branch .LBB0_1389

; __device__ __forceinline__ int ptid() { int t = threadIdx.x; asm volatile("" : "+v"(t)); return t; }
; #define CT_LOADNT(T_) do { const int tt_ = (T_) < CT_TOTAL ? (T_) : CT_TOTAL - 1; const ConvTile ct_ = conv_tile_desc(cttab, tt_); const int ckq_ = lane >> 4, ccol_ = ((lane & 15) * 4 < ct_.nvalid) ? (lane & 15) * 4 : 0; CT_FORQ(CT_LOAD1NT) } while (0)
; __device__ __forceinline__ void ph_glascan(const Params& p, float* lds, int wg, int nwg, int gct_begin) {
;     const unsigned long long* cttab = (const unsigned long long*)((const char*)lds + CTTAB_OFF);
;     bf16_t* ST0 = (bf16_t*)lds; bf16_t* ST1 = ST0 + 32 * GLA_LDP;
;     const int tid = ptid(), w = __builtin_amdgcn_readfirstlane(tid >> 6), lane = tid & 63, r = lane & 15, g = lane >> 4;
;     const int it = w >> 1, vt = w & 1;
;     for (int unit = wg; unit < 256; unit += nwg) {
;         const int bhd = (unit & 7) * 2 + ((unit >> 3) & 1), vs = unit >> 4;
;         const int b = bhd >> 3, h = (bhd >> 1) & 3, dir = bhd & 1;
;         float* const Od = dir ? p.O[1] : p.O[0];
;         for (int q = tid; q < 32 * GLA_LDP / 2; q += NTHR) ((unsigned*)ST0)[q] = 0u;
;         pg8::f32x4 acc[2][2];
; #pragma unroll
;         for (int a = 0; a < 2; ++a)
; #pragma unroll
;             for (int c2 = 0; c2 < 2; ++c2) acc[a][c2] = (pg8::f32x4){0.f, 0.f, 0.f, 0.f};
;         __syncthreads();
;         pg8::bf16x8 cqt[8], cam[2], ckh[2][2], cvt[2][2], nkh[2][2], nvt[2][2]; pg8::f32x4 cdec[2], ndec[2];
;         const pg8::bf16x8 zz = {0, 0, 0, 0, 0, 0, 0, 0};
; #pragma unroll
;         for (int ks = 0; ks < 8; ++ks) cqt[ks] = zz;
; #pragma unroll
;         for (int ks = 0; ks < 2; ++ks) cam[ks] = zz;
;         GLA_LOAD_S(ckh, cvt, cdec, 0);
;         float4 cv0, cv1, cv2, cv3, cv4, cv5, cv6, cv7; CT_LOADNT(gct_begin + wg * 8 + w);
;         const int gct_nch = (CT_TOTAL - gct_begin + nwg * 8 - 1) / (nwg * 8);
.LBB0_1594:
	s_or_b64 exec, exec, s[0:1]
	v_readlane_b32 s0, v248, 43
	v_mov_b32_e32 v4, v0
	v_readlane_b32 s1, v248, 44
	s_waitcnt lgkmcnt(0)
	s_barrier
	s_and_b64 vcc, exec, s[0:1]
	v_readfirstlane_b32 s6, v4
	s_cbranch_vccz .LBB0_1704
	v_writelane_b32 v248, s85, 49
	s_mul_i32 s2, s96, 0x220
	v_readlane_b32 s0, v248, 38
	s_add_i32 s0, s0, s2
	v_readlane_b32 s12, v248, 25
	s_add_i32 s3, s0, s12
	s_ashr_i32 s5, s6, 6
	s_sub_i32 s1, s88, s0
	s_add_i32 s29, s3, s5
	s_add_i32 s1, s1, 0x324ff
	s_ashr_i32 s4, s6, 7
	s_lshl_b32 s0, s5, 5
	s_min_i32 s7, s29, 0x324ff
	s_cmpk_gt_i32 s29, 0x19ff
	s_cselect_b64 s[72:73], -1, 0
	s_cmpk_gt_i32 s29, 0x21ff
	s_cselect_b64 s[74:75], -1, 0
	s_cmpk_gt_i32 s29, 0x4dff
	s_cselect_b64 s[80:81], -1, 0
	s_cmpk_gt_i32 s29, 0x63ff
	s_cselect_b64 s[8:9], -1, 0
	v_writelane_b32 v247, s8, 35
	s_cmpk_gt_i32 s29, 0x7cff
	v_readlane_b32 s13, v248, 26
	v_writelane_b32 v247, s9, 36
	s_cselect_b64 s[8:9], -1, 0
	v_writelane_b32 v248, s8, 53
	s_cmp_gt_i32 s29, 0x84ff
	s_mul_i32 s28, s96, 0x218
	v_writelane_b32 v248, s9, 54
	s_cselect_b64 s[8:9], -1, 0
	s_add_i32 s3, s7, 0xbb00
	s_bfe_u32 s20, s3, 0x6000a
	s_mulk_i32 s20, 0x2493
	s_lshr_b32 s26, s20, 16
	s_mul_i32 s20, s26, 0x1c00
	s_sub_i32 s3, s3, s20
	s_and_b32 s30, s3, 31
	s_bfe_u32 s31, s3, 0xb0005
	s_add_i32 s3, s7, 0xffff7b00
	s_lshr_b32 s20, s3, 11
	s_mul_hi_u32 s34, s20, 0x24924925
	s_mul_i32 s20, s34, 0x3800
	s_sub_i32 s3, s3, s20
	s_bfe_u32 s20, s3, 0x100005
	s_mulk_i32 s20, 0x2493
	s_lshr_b32 s35, s20, 16
	s_mul_i32 s20, s35, 0xe0
	v_writelane_b32 v248, s8, 51
	s_sub_i32 s3, s3, s20
	s_add_i32 s20, s7, 0xffff8300
	v_writelane_b32 v248, s9, 52
	s_lshr_b32 s8, s20, 5
	s_add_i32 s20, s7, 0x9c00
	s_bfe_u32 s21, s20, 0xe0002
	s_mulk_i32 s21, 0x147b
	s_lshr_b32 s27, s21, 17
	s_mul_i32 s21, s27, 0x64
	s_sub_i32 s20, s20, s21
	s_and_b32 s33, s20, 0xffff
	s_add_i32 s20, s7, 0xffffb200
	s_lshr_b32 s45, s20, 5
	s_add_i32 s20, s7, 0xde00
	s_and_b32 s21, s20, 0xffff
	s_mul_i32 s21, s21, 0xba2f
	s_lshr_b32 s47, s21, 23
	s_mul_i32 s21, s47, 0xb0
	s_sub_i32 s20, s20, s21
	s_abs_i32 s21, s88
	v_cvt_f32_u32_e32 v2, s21
	s_and_b32 s65, s20, 0xffff
	s_add_i32 s20, s7, 0xffffe600
	s_lshr_b32 s66, s20, 5
	v_rcp_iflag_f32_e32 v2, v2
	s_mul_hi_i32 s20, s7, 0x4ec4ec4f
	s_lshr_b32 s22, s20, 31
	s_ashr_i32 s67, s20, 5
	v_mul_f32_e32 v2, 0x4f7ffffe, v2
	v_cvt_u32_f32_e32 v2, v2
	s_add_i32 s67, s67, s22
	s_mul_i32 s20, s67, 0x68
	s_sub_i32 s68, s7, s20
	s_sub_i32 s20, 0, s21
	v_readfirstlane_b32 s22, v2
	s_mul_i32 s20, s20, s22
	s_mul_hi_u32 s20, s22, s20
	s_and_b32 s36, s3, 0xffff
	s_and_b32 s3, s7, 31
	s_xor_b32 s7, s1, s88
	s_abs_i32 s1, s1
	s_add_i32 s22, s22, s20
	s_mul_hi_u32 s20, s1, s22
	s_mul_i32 s22, s20, s21
	s_sub_i32 s1, s1, s22
	s_ashr_i32 s7, s7, 31
	s_add_i32 s22, s20, 1
	s_sub_i32 s23, s1, s21
	s_cmp_ge_u32 s1, s21
	s_cselect_b32 s20, s22, s20
	s_cselect_b32 s1, s23, s1
	s_add_i32 s22, s20, 1
	s_cmp_ge_u32 s1, s21
	s_cselect_b32 s1, s22, s20
	s_xor_b32 s1, s1, s7
	s_mov_b32 s69, 5
	s_lshl_b32 s1, s5, 4
	s_and_b32 s70, s6, 0xffffffc0
	s_and_b32 s7, s1, 16
	s_bitcmp1_b32 s5, 0
	s_cselect_b64 s[82:83], -1, 0
	s_ashr_i32 s1, s0, 31
	s_cmp_gt_i32 s29, 0x244ff
	v_writelane_b32 v248, s8, 5
	s_cselect_b64 s[8:9], -1, 0
	v_writelane_b32 v248, s8, 59
	s_and_b64 s[24:25], s[8:9], exec
	s_movk_i32 s25, 0x800
	v_writelane_b32 v248, s9, 60
	s_cselect_b32 s8, s26, s34
	v_writelane_b32 v245, s8, 13
	s_mov_b32 s86, s88
	v_mov_b32_e32 v3, 0
	v_writelane_b32 v245, s9, 14
	s_cselect_b32 s8, s31, s35
	v_writelane_b32 v248, s8, 38
	s_cselect_b32 s8, s30, s36
	v_writelane_b32 v248, s8, 61
	s_cselect_b32 s8, 0x1c00, s25
	v_writelane_b32 v245, s8, 10
	v_and_b32_e32 v2, 48, v4
	v_and_b32_e32 v5, 63, v4
	v_writelane_b32 v245, s9, 11
	s_cselect_b32 s8, s25, 0x1c00
	v_writelane_b32 v245, s8, 12
	s_cselect_b32 s8, 9, 7
	s_add_i32 s44, s70, 0
	s_add_i32 s46, s29, s28
	s_cmpk_gt_i32 s69, 0x43
	s_cselect_b64 s[28:29], -1, 0
	s_min_i32 s50, s46, 0x324ff
	s_cmpk_gt_i32 s46, 0x19ff
	s_cselect_b64 s[30:31], -1, 0
	s_cmpk_gt_u32 s46, 0x21ff
	s_cselect_b64 s[34:35], -1, 0
	s_cmpk_gt_u32 s46, 0x4dff
	v_writelane_b32 v248, s8, 57
	s_cselect_b64 s[8:9], -1, 0
	v_writelane_b32 v248, s8, 45
	s_cmpk_gt_u32 s46, 0x63ff
	v_lshlrev_b32_e32 v159, 3, v5
	v_writelane_b32 v248, s9, 46
	s_cselect_b64 s[8:9], -1, 0
	v_writelane_b32 v248, s8, 47
	s_cmpk_gt_u32 s46, 0x7cff
	v_lshl_or_b32 v8, s5, 11, v159
	v_writelane_b32 v248, s9, 48
	s_cselect_b64 s[8:9], -1, 0
	v_writelane_b32 v245, s8, 3
	s_cmpk_gt_u32 s46, 0x84ff
	v_bfe_u32 v5, v4, 4, 2
	v_writelane_b32 v245, s9, 4
; __device__ __forceinline__ int ptid() { int t = threadIdx.x; asm volatile("" : "+v"(t)); return t; }
; #define CT_LOADNT(T_) do { const int tt_ = (T_) < CT_TOTAL ? (T_) : CT_TOTAL - 1; const ConvTile ct_ = conv_tile_desc(cttab, tt_); const int ckq_ = lane >> 4, ccol_ = ((lane & 15) * 4 < ct_.nvalid) ? (lane & 15) * 4 : 0; CT_FORQ(CT_LOAD1NT) } while (0)
; __device__ __forceinline__ void ph_glascan(const Params& p, float* lds, int wg, int nwg, int gct_begin) {
;     ...
;     const int tid = ptid(), w = __builtin_amdgcn_readfirstlane(tid >> 6), lane = tid & 63, r = lane & 15, g = lane >> 4;
;     const int it = w >> 1, vt = w & 1;
;     for (int unit = wg; unit < 256; unit += nwg) {
;         const int bhd = (unit & 7) * 2 + ((unit >> 3) & 1), vs = unit >> 4;
;         const int b = bhd >> 3, h = (bhd >> 1) & 3, dir = bhd & 1;
;         float* const Od = dir ? p.O[1] : p.O[0];
;         for (int q = tid; q < 32 * GLA_LDP / 2; q += NTHR) ((unsigned*)ST0)[q] = 0u;
;         pg8::f32x4 acc[2][2];
; #pragma unroll
;         for (int a = 0; a < 2; ++a)
; #pragma unroll
;             for (int c2 = 0; c2 < 2; ++c2) acc[a][c2] = (pg8::f32x4){0.f, 0.f, 0.f, 0.f};
;         __syncthreads();
;         pg8::bf16x8 cqt[8], cam[2], ckh[2][2], cvt[2][2], nkh[2][2], nvt[2][2]; pg8::f32x4 cdec[2], ndec[2];
;         const pg8::bf16x8 zz = {0, 0, 0, 0, 0, 0, 0, 0};
; #pragma unroll
;         for (int ks = 0; ks < 8; ++ks) cqt[ks] = zz;
; #pragma unroll
;         for (int ks = 0; ks < 2; ++ks) cam[ks] = zz;
;         GLA_LOAD_S(ckh, cvt, cdec, 0);
;         float4 cv0, cv1, cv2, cv3, cv4, cv5, cv6, cv7; CT_LOADNT(gct_begin + wg * 8 + w);
;         const int gct_nch = (CT_TOTAL - gct_begin + nwg * 8 - 1) / (nwg * 8);
	s_cselect_b64 s[8:9], -1, 0
	s_cmp_lt_u32 s46, 0x24500
	s_cselect_b64 s[48:49], -1, 0
	s_add_i32 s46, s50, 0xbb00
	s_bfe_u32 s51, s46, 0x6000a
	s_mulk_i32 s51, 0x2493
	s_lshr_b32 s51, s51, 16
	s_mul_i32 s52, s51, 0x1c00
	s_sub_i32 s46, s46, s52
	s_add_i32 s52, s50, 0xffff7b00
	s_lshr_b32 s53, s52, 11
	s_mul_hi_u32 s53, s53, 0x24924925
	s_mul_i32 s54, s53, 0x3800
	s_sub_i32 s52, s52, s54
	s_bfe_u32 s54, s52, 0x100005
	s_mulk_i32 s54, 0x2493
	s_lshr_b32 s54, s54, 16
	s_mul_i32 s55, s54, 0xe0
	s_sub_i32 s52, s52, s55
	s_add_i32 s55, s50, 0x9c00
	s_bfe_u32 s56, s55, 0xe0002
	s_mulk_i32 s56, 0x147b
	s_lshr_b32 s79, s56, 17
	s_mul_i32 s56, s79, 0x64
	s_sub_i32 s55, s55, s56
	s_add_i32 s56, s50, 0xde00
	s_and_b32 s57, s56, 0xffff
	s_mul_i32 s57, s57, 0xba2f
	s_lshr_b32 s76, s57, 23
	s_mul_i32 s57, s76, 0xb0
	s_sub_i32 s56, s56, s57
	s_mul_hi_i32 s57, s50, 0x4ec4ec4f
	s_lshr_b32 s58, s57, 31
	s_ashr_i32 s77, s57, 5
	v_writelane_b32 v248, s8, 55
	s_add_i32 s77, s77, s58
	s_add_i32 s58, s50, 0xffff8300
	v_writelane_b32 v248, s9, 56
	s_lshr_b32 s8, s58, 5
	v_writelane_b32 v245, s8, 9
	s_and_b32 s8, s55, 0xffff
	s_add_i32 s55, s50, 0xffffb200
	s_lshr_b32 s26, s55, 5
	s_mul_i32 s55, s77, 0x68
	s_sub_i32 s87, s50, s55
	s_and_b32 s24, s50, 31
	s_addk_i32 s50, 0xe600
	s_and_b32 s57, s46, 31
	s_bfe_u32 s46, s46, 0xb0005
	s_and_b32 s52, s52, 0xffff
	s_and_b32 s71, s56, 0xffff
	s_lshr_b32 s88, s50, 5
	v_cndmask_b32_e64 v158, 0, 1, s[48:49]
	s_and_b64 s[48:49], s[48:49], exec
	v_writelane_b32 v248, s8, 63
	s_cselect_b32 s8, s52, s57
	v_writelane_b32 v245, s8, 1
	s_cselect_b32 s8, s54, s46
	v_writelane_b32 v245, s8, 6
	s_cselect_b32 s8, s53, s51
	v_writelane_b32 v245, s8, 7
	v_readlane_b32 s36, v248, 29
	v_readlane_b32 s38, v248, 31
	v_writelane_b32 v245, s9, 8
	s_cselect_b32 s8, 16, 17
	v_writelane_b32 v245, s8, 15
	s_cselect_b32 s8, 0x1c00, s25
	v_writelane_b32 v245, s8, 5
	s_cselect_b32 s8, s25, 0x1c00
	v_writelane_b32 v245, s8, 17
	v_readlane_b32 s39, v248, 32
	s_lshl_b32 s6, s6, 3
	v_writelane_b32 v245, s9, 18
	v_readlane_b32 s8, v248, 37
	s_add_i32 s25, s5, s8
	s_add_i32 s89, s25, s12
	v_lshl_add_u64 v[6:7], s[38:39], 0, v[2:3]
	s_lshl_b64 s[0:1], s[0:1], 2
	s_addk_i32 s89, 0x6400
	s_and_b32 s6, s6, 0xfffffc00
	s_lshl_b32 s94, s90, 1
	s_lshl_b32 s95, s96, 1
	v_lshl_add_u64 v[160:161], v[6:7], 0, s[0:1]
	s_add_u32 s0, s38, s0
	v_or_b32_e32 v10, s6, v159
	v_and_b32_e32 v11, 15, v4
	v_readlane_b32 s48, v248, 9
	s_addc_u32 s1, s39, s1
	v_lshlrev_b32_e32 v162, 3, v5
	v_lshl_or_b32 v13, s4, 4, v11
	v_lshl_or_b32 v12, s4, 12, v159
	v_lshlrev_b32_e32 v14, 2, v5
	v_lshlrev_b32_e32 v164, 2, v11
	v_or_b32_e32 v5, s7, v11
	v_ashrrev_i32_e32 v9, 31, v8
	v_mul_u32_u24_e32 v197, 0x210, v11
	v_readlane_b32 s49, v248, 10
	v_readlane_b32 s50, v248, 11
	v_readlane_b32 s51, v248, 12
	v_readlane_b32 s60, v248, 21
	v_readlane_b32 s61, v248, 22
	v_readlane_b32 s62, v248, 23
	v_readlane_b32 s63, v248, 24
	v_ashrrev_i32_e32 v11, 31, v10
	v_readlane_b32 s37, v248, 30
	s_mov_b64 s[84:85], s[96:97]
	v_lshl_add_u64 v[6:7], s[0:1], 0, v[2:3]
	v_add_u32_e32 v15, s44, v162
	v_mul_u32_u24_e32 v196, 0x210, v5
	v_add_u32_e32 v199, 0xfc0, v13
	v_sub_u32_e32 v200, 63, v13
	v_readlane_b32 s53, v248, 14
	v_readlane_b32 s58, v248, 19
	v_readlane_b32 s59, v248, 20
	v_lshl_add_u64 v[166:167], v[8:9], 1, s[60:61]
	v_add_u32_e32 v203, 0xffffff00, v13
	v_sub_u32_e32 v204, 0x10ff, v13
	v_lshl_add_u64 v[8:9], v[10:11], 1, s[62:63]
	s_mov_b64 s[48:49], 0x2000
	s_mov_b64 s[50:51], 0x400
	v_ashrrev_i32_e32 v13, 31, v12
	s_add_u32 s96, s36, 0x10000
	s_movk_i32 s0, 0x1080
	v_or_b32_e32 v189, 1, v162
	v_or_b32_e32 v190, 2, v162
	v_or_b32_e32 v191, 3, v162
	v_or_b32_e32 v192, 4, v162
	v_or_b32_e32 v193, 5, v162
	v_or_b32_e32 v194, 6, v162
	v_or_b32_e32 v195, 7, v162
	v_add3_u32 v198, 0, v196, v2
	v_add_u32_e32 v201, 0xfffffe00, v4
	v_lshl_add_u32 v202, v4, 2, 0
	v_lshl_add_u64 v[168:169], v[8:9], 0, s[48:49]
	v_lshl_add_u64 v[170:171], v[6:7], 0, s[50:51]
	v_lshl_add_u64 v[172:173], v[12:13], 1, s[58:59]
	s_addc_u32 s97, s37, 0
	s_lshl_b32 s4, s7, 2
	v_lshlrev_b32_e32 v174, 2, v14
	v_add_u32_e32 v205, v15, v197
	v_cmp_gt_i32_e64 s[0:1], s0, v4
	s_add_i32 s5, 0, 0x4200
	s_mov_b64 s[38:39], s[90:91]
	s_mov_b32 s64, s90
	s_mov_b32 s53, 0
	v_readlane_b32 s40, v248, 33
	v_readlane_b32 s41, v248, 34
	v_readlane_b32 s42, v248, 35
	v_readlane_b32 s43, v248, 36
	v_readlane_b32 s52, v248, 13
	v_readlane_b32 s54, v248, 15
	v_readlane_b32 s55, v248, 16
	v_readlane_b32 s56, v248, 17
	v_readlane_b32 s57, v248, 18
	s_branch .LBB0_1599

; #define CT_LOADNT(T_) do { const int tt_ = (T_) < CT_TOTAL ? (T_) : CT_TOTAL - 1; const ConvTile ct_ = conv_tile_desc(cttab, tt_); const int ckq_ = lane >> 4, ccol_ = ((lane & 15) * 4 < ct_.nvalid) ? (lane & 15) * 4 : 0; CT_FORQ(CT_LOAD1NT) } while (0)
; #define CT_STORENT(T_) do { const int tt_ = (T_) < CT_TOTAL ? (T_) : CT_TOTAL - 1; const ConvTile ct_ = conv_tile_desc(cttab, tt_); const bool cok_ = (lane & 15) * 4 < ct_.nvalid; \
;     bf16_t* cdst_ = ct_.dst + (size_t)((lane & 15) * 4) * ct_.K + (lane >> 4) * 8; CT_ATOMNT(0, x) CT_ATOMNT(1, y) CT_ATOMNT(2, z) CT_ATOMNT(3, w) } while (0)
; __device__ __forceinline__ void ph_glascan(const Params& p, float* lds, int wg, int nwg, int gct_begin) {
;     ...
;             {
;                 const int tconv = gct_begin + c * (nwg * 8) + wg * 8 + w;
;                 if (c < gct_nch) { CT_STORENT(tconv); if (c + 1 < gct_nch) CT_LOADNT(tconv + nwg * 8); }
;             }
.LBB0_1597:
	s_lshl_b32 s46, s46, 6
	s_sub_i32 s52, s25, s46
	s_and_b64 s[56:57], s[56:57], exec
	s_cselect_b32 s52, 64, s52
	s_lshl_b32 s44, s44, 3
	s_add_i32 s44, s44, 0
	s_add_i32 s44, s44, 0x20040
	v_mov_b32_e32 v2, s44
	ds_read_b64 v[6:7], v2
	s_mul_i32 s25, s6, s25
	v_lshlrev_b32_e64 v2, v4, s25
	v_mul_hi_u32 v5, v2, s54
	v_mul_lo_u32 v4, v2, s54
	s_lshl_b32 s56, s7, 5
	v_lshlrev_b64 v[4:5], 1, v[4:5]
	s_mul_hi_i32 s55, s6, s46
	s_mul_i32 s54, s6, s46
	s_ashr_i32 s57, s56, 31
	s_waitcnt lgkmcnt(0)
	v_lshl_add_u64 v[4:5], v[6:7], 0, v[4:5]
	s_lshl_b64 s[54:55], s[54:55], 1
	v_lshl_add_u64 v[4:5], v[4:5], 0, s[54:55]
	s_lshl_b64 s[54:55], s[56:57], 1
	v_mul_u32_u24_e32 v2, s6, v164
	v_lshl_add_u64 v[4:5], v[4:5], 0, s[54:55]
	v_lshlrev_b32_e32 v2, 1, v2
	v_lshl_add_u64 v[4:5], v[4:5], 0, v[2:3]
	v_lshlrev_b32_e32 v2, 1, v162
	v_lshl_add_u64 v[8:9], v[4:5], 0, v[2:3]
	v_cvt_pk_bf16_f32 v2, v74, v78
	v_cvt_pk_bf16_f32 v4, v86, v94
	v_cvt_pk_bf16_f32 v5, v102, v114
	v_cvt_pk_bf16_f32 v6, v126, v130
	v_cmp_gt_i32_e32 vcc, s52, v164
	s_lshl_b32 s52, s6, 1
	s_nop 0
	v_cndmask_b32_e32 v7, 0, v6, vcc
	v_cndmask_b32_e32 v6, 0, v5, vcc
	v_cndmask_b32_e32 v5, 0, v4, vcc
	v_cndmask_b32_e32 v4, 0, v2, vcc
	global_store_dwordx4 v[8:9], v[4:7], off nt
	v_cvt_pk_bf16_f32 v2, v75, v79
	v_lshl_add_u64 v[8:9], v[8:9], 0, s[52:53]
	v_cvt_pk_bf16_f32 v4, v87, v95
	v_cvt_pk_bf16_f32 v5, v103, v115
	v_cvt_pk_bf16_f32 v6, v127, v131
	v_cndmask_b32_e32 v7, 0, v6, vcc
	v_cndmask_b32_e32 v6, 0, v5, vcc
	v_cndmask_b32_e32 v5, 0, v4, vcc
	v_cndmask_b32_e32 v4, 0, v2, vcc
	global_store_dwordx4 v[8:9], v[4:7], off nt
	v_cvt_pk_bf16_f32 v2, v76, v80
	v_lshl_add_u64 v[8:9], v[8:9], 0, s[52:53]
	v_cvt_pk_bf16_f32 v4, v88, v96
	v_cvt_pk_bf16_f32 v5, v104, v116
	v_cvt_pk_bf16_f32 v6, v128, v132
	v_cndmask_b32_e32 v7, 0, v6, vcc
	v_cndmask_b32_e32 v6, 0, v5, vcc
	v_cndmask_b32_e32 v5, 0, v4, vcc
	v_cndmask_b32_e32 v4, 0, v2, vcc
	global_store_dwordx4 v[8:9], v[4:7], off nt
	v_cvt_pk_bf16_f32 v2, v77, v81
	v_lshl_add_u64 v[8:9], v[8:9], 0, s[52:53]
	v_cvt_pk_bf16_f32 v4, v89, v97
	v_cvt_pk_bf16_f32 v5, v105, v117
	v_cvt_pk_bf16_f32 v6, v129, v133
	v_cndmask_b32_e32 v7, 0, v6, vcc
	v_cndmask_b32_e32 v6, 0, v5, vcc
	v_cndmask_b32_e32 v5, 0, v4, vcc
	v_cndmask_b32_e32 v4, 0, v2, vcc
	global_store_dwordx4 v[8:9], v[4:7], off nt

; #define CT_LOADNT(T_) do { const int tt_ = (T_) < CT_TOTAL ? (T_) : CT_TOTAL - 1; const ConvTile ct_ = conv_tile_desc(cttab, tt_); const int ckq_ = lane >> 4, ccol_ = ((lane & 15) * 4 < ct_.nvalid) ? (lane & 15) * 4 : 0; CT_FORQ(CT_LOAD1NT) } while (0)
; __device__ __forceinline__ void ph_glascan(const Params& p, float* lds, int wg, int nwg, int gct_begin) {
;     ...
;     for (int unit = wg; unit < 256; unit += nwg) {
;         const int bhd = (unit & 7) * 2 + ((unit >> 3) & 1), vs = unit >> 4;
;         const int b = bhd >> 3, h = (bhd >> 1) & 3, dir = bhd & 1;
;         float* const Od = dir ? p.O[1] : p.O[0];
;         for (int q = tid; q < 32 * GLA_LDP / 2; q += NTHR) ((unsigned*)ST0)[q] = 0u;
;         pg8::f32x4 acc[2][2];
; #pragma unroll
;         for (int a = 0; a < 2; ++a)
; #pragma unroll
;             for (int c2 = 0; c2 < 2; ++c2) acc[a][c2] = (pg8::f32x4){0.f, 0.f, 0.f, 0.f};
;         __syncthreads();
;         pg8::bf16x8 cqt[8], cam[2], ckh[2][2], cvt[2][2], nkh[2][2], nvt[2][2]; pg8::f32x4 cdec[2], ndec[2];
;         const pg8::bf16x8 zz = {0, 0, 0, 0, 0, 0, 0, 0};
; #pragma unroll
;         for (int ks = 0; ks < 8; ++ks) cqt[ks] = zz;
; #pragma unroll
;         for (int ks = 0; ks < 2; ++ks) cam[ks] = zz;
;         GLA_LOAD_S(ckh, cvt, cdec, 0);
;         float4 cv0, cv1, cv2, cv3, cv4, cv5, cv6, cv7; CT_LOADNT(gct_begin + wg * 8 + w);
.LBB0_1615:
	s_lshr_b32 s7, s64, 3
	s_bfe_u32 s46, s94, 0x30001
	s_and_b32 s7, s7, 1
	s_mulk_i32 s46, 0x88
	s_mulk_i32 s7, 0x44
	s_add_i32 s7, s46, s7
	s_lshl_b32 s52, s7, 13
	v_lshl_add_u64 v[176:177], v[168:169], 0, s[52:53]
	s_lshl_b32 s52, s7, 10
	v_lshl_add_u64 v[178:179], v[170:171], 0, s[52:53]
	s_lshl_b32 s46, s7, 16
	s_lshl_b32 s52, s7, 15
	s_cmp_eq_u32 s6, 0
	s_cselect_b64 s[6:7], -1, 0
	v_readlane_b32 s8, v248, 9
	s_and_b64 vcc, s[6:7], exec
	v_readlane_b32 s14, v248, 15
	v_readlane_b32 s15, v248, 16
	v_readlane_b32 s16, v248, 17
	v_readlane_b32 s17, v248, 18
	v_lshl_add_u64 v[180:181], v[166:167], 0, s[52:53]
	v_lshl_add_u64 v[182:183], v[172:173], 0, s[52:53]
	s_cselect_b32 s52, s15, s17
	s_cselect_b32 s93, s14, s16
	s_lshl_b32 s57, s92, 6
	s_lshl_b32 vcc_lo, s92, 5
	s_and_b32 vcc_lo, vcc_lo, 0xffffff80
	s_and_b32 vcc_hi, s57, 64
	s_or_b32 vcc_lo, vcc_lo, vcc_hi
	s_bfe_u32 s92, s92, 0x10001
	s_and_b64 s[62:63], s[62:63], exec
	s_cselect_b32 vcc_lo, s57, vcc_lo
	s_cselect_b32 s92, 0, s92
	s_sub_i32 s57, s25, s57
	s_cmp_gt_i32 s57, 0
	s_cselect_b64 s[62:63], -1, 0
	s_or_b64 s[62:63], s[60:61], s[62:63]
	s_and_b64 s[60:61], s[60:61], exec
	s_cselect_b32 s60, 64, s57
	s_lshl_b32 s57, s91, 3
	s_add_i32 s57, s57, 0
	s_lshl_b32 s61, s92, 3
	s_add_i32 s57, s57, s61
	s_add_i32 s57, s57, 0x20040
	v_mov_b32_e32 v2, s57
	ds_read_b64 v[30:31], v2
	s_mul_i32 s56, s58, s56
	s_mul_hi_u32 s57, s56, s25
	s_mul_i32 s56, s56, s25
	s_lshl_b64 s[56:57], s[56:57], 2
	s_waitcnt lgkmcnt(0)
	v_lshl_add_u64 v[30:31], v[30:31], 0, s[56:57]
	s_lshl_b32 s56, s59, 5
	s_mul_hi_i32 s57, s25, s56
	s_mul_i32 s56, s25, s56
	s_lshl_b64 s[56:57], s[56:57], 2
	s_ashr_i32 s58, vcc_lo, 31
	v_lshl_add_u64 v[30:31], v[30:31], 0, s[56:57]
	s_and_b64 s[56:57], s[62:63], exec
	s_cselect_b32 s57, s58, 0
	s_cselect_b32 s56, vcc_lo, 0
	s_lshl_b64 s[56:57], s[56:57], 2
	v_mul_u32_u24_e32 v2, s25, v162
	v_lshl_add_u64 v[30:31], v[30:31], 0, s[56:57]
	v_cmp_gt_i32_e32 vcc, s60, v164
	v_lshlrev_b32_e32 v2, 2, v2
	v_lshl_add_u64 v[32:33], v[30:31], 0, v[2:3]
	v_cndmask_b32_e32 v2, 0, v164, vcc
	v_lshlrev_b32_e32 v2, 2, v2
	v_lshl_add_u64 v[32:33], v[32:33], 0, v[2:3]
	global_load_dwordx4 v[74:77], v[32:33], off nt
	v_mul_u32_u24_e32 v32, s25, v189
	v_lshlrev_b32_e32 v32, 2, v32
	v_mov_b32_e32 v33, v3
	v_lshl_add_u64 v[32:33], v[30:31], 0, v[32:33]
	v_lshl_add_u64 v[32:33], v[32:33], 0, v[2:3]
	global_load_dwordx4 v[78:81], v[32:33], off nt
	v_mul_u32_u24_e32 v32, s25, v190
	v_lshlrev_b32_e32 v32, 2, v32
	v_mov_b32_e32 v33, v3
	v_lshl_add_u64 v[32:33], v[30:31], 0, v[32:33]
	v_lshl_add_u64 v[32:33], v[32:33], 0, v[2:3]
	global_load_dwordx4 v[86:89], v[32:33], off nt
	v_mul_u32_u24_e32 v32, s25, v191
	v_lshlrev_b32_e32 v32, 2, v32
	v_mov_b32_e32 v33, v3
	v_lshl_add_u64 v[32:33], v[30:31], 0, v[32:33]
	v_lshl_add_u64 v[32:33], v[32:33], 0, v[2:3]
	global_load_dwordx4 v[94:97], v[32:33], off nt
	v_mul_u32_u24_e32 v32, s25, v192
	v_lshlrev_b32_e32 v32, 2, v32
	v_mov_b32_e32 v33, v3
	v_lshl_add_u64 v[32:33], v[30:31], 0, v[32:33]
	v_lshl_add_u64 v[32:33], v[32:33], 0, v[2:3]
	global_load_dwordx4 v[102:105], v[32:33], off nt
	v_mul_u32_u24_e32 v32, s25, v193
	v_lshlrev_b32_e32 v32, 2, v32
	v_mov_b32_e32 v33, v3
	v_lshl_add_u64 v[32:33], v[30:31], 0, v[32:33]
	v_lshl_add_u64 v[32:33], v[32:33], 0, v[2:3]
	global_load_dwordx4 v[114:117], v[32:33], off nt
	v_mul_u32_u24_e32 v32, s25, v194
	v_lshlrev_b32_e32 v32, 2, v32
	v_mov_b32_e32 v33, v3
	v_lshl_add_u64 v[32:33], v[30:31], 0, v[32:33]
	v_lshl_add_u64 v[32:33], v[32:33], 0, v[2:3]
	global_load_dwordx4 v[126:129], v[32:33], off nt
	v_mul_u32_u24_e32 v32, s25, v195
	v_lshlrev_b32_e32 v32, 2, v32
	v_mov_b32_e32 v33, v3
	v_lshl_add_u64 v[30:31], v[30:31], 0, v[32:33]
	v_lshl_add_u64 v[30:31], v[30:31], 0, v[2:3]
	global_load_dwordx4 v[130:133], v[30:31], off nt
	s_lshl_b32 s25, s78, 9
	s_and_b32 s78, s25, 0x1000
	s_lshl_b32 s25, s64, 11
	s_and_b32 s25, s25, 0x1800
	s_add_u32 s25, s93, s25
	s_addc_u32 s52, s52, 0
	s_lshl_b32 s56, s44, 5
	s_ashr_i32 s57, s56, 31
	s_lshl_b64 s[56:57], s[56:57], 2
	s_add_u32 s25, s25, s56
	s_addc_u32 s44, s52, s57
	s_add_u32 s56, s25, s4
	s_addc_u32 s57, s44, 0
	v_mov_b32_e32 v175, v3
	v_lshl_add_u64 v[184:185], s[56:57], 0, v[174:175]
	s_add_u32 s56, s96, s46
	s_addc_u32 s57, s97, 0
	v_lshl_add_u64 v[186:187], v[4:5], 1, s[56:57]
	v_mov_b32_e32 v4, v3
	v_mov_b32_e32 v5, v3
	v_mov_b32_e32 v2, v3
	v_mov_b32_e32 v30, 0
	v_mov_b32_e32 v66, 0
	v_mov_b64_e32 v[36:37], v[4:5]
	v_mov_b64_e32 v[40:41], v[4:5]
	v_mov_b64_e32 v[44:45], v[4:5]
	v_mov_b64_e32 v[52:53], v[4:5]
	v_mov_b64_e32 v[48:49], v[4:5]
	v_mov_b64_e32 v[56:57], v[4:5]
	v_mov_b64_e32 v[60:61], v[4:5]
	v_mov_b64_e32 v[64:65], v[4:5]
	s_mov_b32 s93, s89
	v_mov_b32_e32 v175, v204
	v_mov_b32_e32 v206, v203
	v_mov_b64_e32 v[34:35], v[2:3]
	v_mov_b64_e32 v[38:39], v[2:3]
	v_mov_b64_e32 v[42:43], v[2:3]
	v_mov_b64_e32 v[50:51], v[2:3]
	v_mov_b64_e32 v[46:47], v[2:3]
	v_mov_b64_e32 v[54:55], v[2:3]
	v_mov_b64_e32 v[58:59], v[2:3]
	v_mov_b64_e32 v[62:63], v[2:3]
	v_mov_b32_e32 v67, v66
	v_mov_b32_e32 v68, v66
	v_mov_b32_e32 v69, v66
	v_mov_b32_e32 v82, v66
	v_mov_b32_e32 v83, v66
	v_mov_b32_e32 v84, v66
	v_mov_b32_e32 v85, v66
	v_mov_b32_e32 v90, v66
	v_mov_b32_e32 v91, v66
	v_mov_b32_e32 v92, v66
	v_mov_b32_e32 v93, v66
	v_mov_b32_e32 v98, v66
	v_mov_b32_e32 v99, v66
	v_mov_b32_e32 v100, v66
	v_mov_b32_e32 v101, v66
	v_mov_b32_e32 v31, v30
	v_mov_b32_e32 v32, v30
	v_mov_b32_e32 v33, v30
	v_mov_b32_e32 v70, v30
	v_mov_b32_e32 v71, v30
	v_mov_b32_e32 v72, v30
	v_mov_b32_e32 v73, v30
	v_readlane_b32 s9, v248, 10
	v_readlane_b32 s10, v248, 11
	v_readlane_b32 s11, v248, 12
	v_readlane_b32 s12, v248, 13
	v_readlane_b32 s13, v248, 14
	v_readlane_b32 s18, v248, 19
	v_readlane_b32 s19, v248, 20
	v_readlane_b32 s20, v248, 21
	v_readlane_b32 s21, v248, 22
	v_readlane_b32 s22, v248, 23
	v_readlane_b32 s23, v248, 24
	s_waitcnt vmcnt(0)
; __device__ __forceinline__ unsigned cvt_pk_bf16(float lo, float hi) { const f32x2_t v = {lo, hi}; return __builtin_bit_cast(unsigned, __builtin_convertvector(v, bf16x2_t)); }
; __device__ __forceinline__ void ph_glascan(const Params& p, float* lds, int wg, int nwg, int gct_begin) {
;     ...
;         for (int c = 0; c < GLA_NCH; ++c) {
;             GLA_LOAD_S(nkh, nvt, ndec, c + 1);
;             bf16_t* STc = (c & 1) ? ST1 : ST0; bf16_t* STn = (c & 1) ? ST0 : ST1;
; #pragma unroll
;             for (int dt = 0; dt < 2; ++dt)
; #pragma unroll
;                 for (int v2 = 0; v2 < 2; ++v2) {
;                     pg8::f32x4 a = acc[dt][v2] * cdec[dt];
; #pragma unroll
;                     for (int ks = 0; ks < 2; ++ks) a = __builtin_amdgcn_mfma_f32_16x16x32_bf16(ckh[dt][ks], cvt[v2][ks], a, 0, 0, 0);
;                     acc[dt][v2] = a;
;                     uint2 sv; sv.x = cvt_pk_bf16(a[0], a[1]); sv.y = cvt_pk_bf16(a[2], a[3]);
;                     *(uint2*)(STn + (v2 * 16 + r) * GLA_LDP + (2 * w + dt) * 16 + 4 * g) = sv;
;                 }
;             if (c >= 4) {
;                 pg8::f32x4 o = {0.f, 0.f, 0.f, 0.f};
; #pragma unroll
;                 for (int ks = 0; ks < 8; ++ks) { const pg8::bf16x8 sa = *(const pg8::bf16x8*)(STc + (vt * 16 + r) * GLA_LDP + ks * 32 + 8 * g);
;                     o = __builtin_amdgcn_mfma_f32_16x16x32_bf16(sa, cqt[ks], o, 0, 0, 0); }
;                 if (vt == 0) {
; #pragma unroll
;                     for (int ks = 0; ks < 2; ++ks) o = __builtin_amdgcn_mfma_f32_16x16x32_bf16(cvt[0][ks], cam[ks], o, 0, 0, 0);
;                 } else {
; #pragma unroll
;                     for (int ks = 0; ks < 2; ++ks) o = __builtin_amdgcn_mfma_f32_16x16x32_bf16(cvt[1][ks], cam[ks], o, 0, 0, 0);
;                 }
.LBB0_1616:
	v_lshl_add_u64 v[4:5], v[180:181], 0, s[54:55]
	s_mov_b32 s25, 0x8000
	v_add_co_u32_e32 v4, vcc, s25, v4
	v_mov_b64_e32 v[210:211], v[16:17]
	v_mov_b64_e32 v[214:215], v[20:21]
	v_mov_b64_e32 v[218:219], v[12:13]
	v_mov_b64_e32 v[222:223], v[8:9]
	v_addc_co_u32_e32 v5, vcc, 0, v5, vcc
	v_mov_b64_e32 v[208:209], v[14:15]
	v_mov_b64_e32 v[212:213], v[18:19]
	v_mov_b64_e32 v[216:217], v[10:11]
	v_mov_b64_e32 v[220:221], v[6:7]
	global_load_dwordx4 v[14:17], v[4:5], off
	global_load_dwordx4 v[18:21], v[4:5], off offset:1024
	global_load_dwordx4 v[106:109], v[186:187], off
	global_load_dwordx4 v[110:113], v[186:187], off offset:1024
	global_load_dwordx4 v[10:13], v[4:5], off offset:2048
	global_load_dwordx4 v[6:9], v[4:5], off offset:3072
	global_load_dwordx4 v[122:125], v[186:187], off offset:2048
	global_load_dwordx4 v[118:121], v[186:187], off offset:3072
	v_mov_b64_e32 v[156:157], v[28:29]
	v_mov_b64_e32 v[152:153], v[24:25]
	v_mov_b64_e32 v[154:155], v[26:27]
	v_mov_b64_e32 v[150:151], v[22:23]
	v_pk_mul_f32 v[24:25], v[100:101], v[156:157]
	v_pk_mul_f32 v[22:23], v[98:99], v[154:155]
	v_pk_mul_f32 v[84:85], v[84:85], v[152:153]
	v_pk_mul_f32 v[82:83], v[82:83], v[150:151]
	v_mfma_f32_16x16x32_bf16 v[98:101], v[208:211], v[138:141], v[22:25]
	global_load_dwordx4 v[26:29], v[178:179], off
	s_nop 1
	global_load_dwordx4 v[22:25], v[178:179], off offset:64
	v_pk_mul_f32 v[92:93], v[92:93], v[156:157]
	v_pk_mul_f32 v[90:91], v[90:91], v[154:155]
	v_mfma_f32_16x16x32_bf16 v[82:85], v[216:219], v[138:141], v[82:85]
	v_mul_f32_e64 v68, v68, v152
	v_mul_f32_e64 v69, v69, v153
	v_pk_mul_f32 v[66:67], v[66:67], v[150:151]
	s_bitcmp0_b32 s90, 0
	v_mfma_f32_16x16x32_bf16 v[90:93], v[208:211], v[146:149], v[90:93]
	s_cselect_b64 s[56:57], -1, 0
	s_and_b64 s[58:59], s[56:57], exec
	s_cselect_b32 s25, s5, 0
	v_mfma_f32_16x16x32_bf16 v[66:69], v[216:219], v[146:149], v[66:69]
	s_add_i32 s25, s25, s70
	v_add3_u32 v2, s25, v162, v197
	s_cmp_lt_u32 s90, 4
	v_mfma_f32_16x16x32_bf16 v[98:101], v[212:215], v[134:137], v[98:101]
	v_mfma_f32_16x16x32_bf16 v[82:85], v[220:223], v[134:137], v[82:85]
	v_mfma_f32_16x16x32_bf16 v[90:93], v[212:215], v[142:145], v[90:93]
	s_nop 5
	v_cvt_pk_bf16_f32 v4, v98, v99
	v_cvt_pk_bf16_f32 v5, v100, v101
	v_cvt_pk_bf16_f32 v150, v82, v83
	v_mfma_f32_16x16x32_bf16 v[66:69], v[220:223], v[142:145], v[66:69]
	v_cvt_pk_bf16_f32 v151, v84, v85
	v_cvt_pk_bf16_f32 v154, v90, v91
	v_cvt_pk_bf16_f32 v155, v92, v93
	ds_write2_b64 v2, v[4:5], v[150:151] offset1:4
	v_add_u32_e32 v2, 0x2000, v2
	s_nop 2
	v_cvt_pk_bf16_f32 v4, v66, v67
	v_cvt_pk_bf16_f32 v5, v68, v69
	ds_write2_b64 v2, v[154:155], v[4:5] offset0:32 offset1:36
	s_cbranch_scc1 .LBB0_1623
	s_and_b64 s[56:57], s[56:57], exec
	s_cselect_b32 s25, 0, s5
	v_lshlrev_b32_e32 v2, 1, v162
	v_add3_u32 v2, s25, v196, v2
	ds_read_b128 v[150:153], v2
	ds_read_b128 v[154:157], v2 offset:64
	s_mov_b64 s[56:57], -1
	s_andn2_b64 vcc, exec, s[82:83]
	s_waitcnt lgkmcnt(0)
	s_cmp_lt_i32 s90, s69
	s_cbranch_scc1 .Lgla_o_ok
	s_waitcnt vmcnt(10)
.Lgla_o_ok:
	v_mfma_f32_16x16x32_bf16 v[150:153], v[150:153], v[62:65], 0
	v_mfma_f32_16x16x32_bf16 v[150:153], v[154:157], v[58:61], v[150:153]
	ds_read_b128 v[154:157], v2 offset:128
	s_waitcnt lgkmcnt(0)
	v_mfma_f32_16x16x32_bf16 v[150:153], v[154:157], v[54:57], v[150:153]
	ds_read_b128 v[154:157], v2 offset:192
	s_waitcnt lgkmcnt(0)
	v_mfma_f32_16x16x32_bf16 v[150:153], v[154:157], v[46:49], v[150:153]
	ds_read_b128 v[154:157], v2 offset:256
	s_waitcnt lgkmcnt(0)
	v_mfma_f32_16x16x32_bf16 v[150:153], v[154:157], v[50:53], v[150:153]
	ds_read_b128 v[154:157], v2 offset:320
	s_waitcnt lgkmcnt(0)
	v_mfma_f32_16x16x32_bf16 v[150:153], v[154:157], v[42:45], v[150:153]
	ds_read_b128 v[154:157], v2 offset:384
	s_waitcnt lgkmcnt(0)
	v_mfma_f32_16x16x32_bf16 v[150:153], v[154:157], v[38:41], v[150:153]
	ds_read_b128 v[154:157], v2 offset:448
	s_waitcnt lgkmcnt(0)
	v_mfma_f32_16x16x32_bf16 v[150:153], v[154:157], v[34:37], v[150:153]
	s_cbranch_vccnz .LBB0_1619
	v_mfma_f32_16x16x32_bf16 v[146:149], v[146:149], v[30:33], v[150:153]
	s_mov_b64 s[56:57], 0
	v_mfma_f32_16x16x32_bf16 v[154:157], v[142:145], v[70:73], v[146:149]

; #define CT_LOADNT(T_) do { const int tt_ = (T_) < CT_TOTAL ? (T_) : CT_TOTAL - 1; const ConvTile ct_ = conv_tile_desc(cttab, tt_); const int ckq_ = lane >> 4, ccol_ = ((lane & 15) * 4 < ct_.nvalid) ? (lane & 15) * 4 : 0; CT_FORQ(CT_LOAD1NT) } while (0)
; #define CT_STORENT(T_) do { const int tt_ = (T_) < CT_TOTAL ? (T_) : CT_TOTAL - 1; const ConvTile ct_ = conv_tile_desc(cttab, tt_); const bool cok_ = (lane & 15) * 4 < ct_.nvalid; \
;     bf16_t* cdst_ = ct_.dst + (size_t)((lane & 15) * 4) * ct_.K + (lane >> 4) * 8; CT_ATOMNT(0, x) CT_ATOMNT(1, y) CT_ATOMNT(2, z) CT_ATOMNT(3, w) } while (0)
; __device__ __forceinline__ void ph_glascan(const Params& p, float* lds, int wg, int nwg, int gct_begin) {
;     ...
;             {
;                 const int tconv = gct_begin + c * (nwg * 8) + wg * 8 + w;
;                 if (c < gct_nch) { CT_STORENT(tconv); if (c + 1 < gct_nch) CT_LOADNT(tconv + nwg * 8); }
;             }
.LBB0_1652:
	s_lshl_b32 s62, s91, 6
	s_sub_i32 s52, s25, s62
	s_and_b64 s[58:59], s[58:59], exec
	s_cselect_b32 s63, 64, s52
	s_mul_i32 s52, s56, s25
	s_lshl_b32 s25, s92, 3
	s_add_i32 s25, s25, 0
	s_add_i32 s25, s25, 0x20040
	v_mov_b32_e32 v2, s25
	ds_read_b64 v[4:5], v2
	s_lshl_b64 s[58:59], s[52:53], s60
	s_mul_i32 s25, s59, s46
	s_mul_hi_u32 s52, s58, s46
	s_add_i32 s59, s52, s25
	s_ashr_i32 s25, s62, 31
	s_mul_i32 s58, s58, s46
	s_mul_i32 s25, s56, s25
	s_mul_hi_u32 s46, s56, s62
	s_lshl_b64 s[58:59], s[58:59], 1
	s_add_i32 s25, s46, s25
	s_mul_i32 s46, s57, s62
	s_lshl_b32 s60, s90, 5
	s_waitcnt lgkmcnt(0)
	v_lshl_add_u64 v[4:5], v[4:5], 0, s[58:59]
	s_add_i32 s59, s25, s46
	s_mul_i32 s58, s56, s62
	s_ashr_i32 s61, s60, 31
	s_lshl_b64 s[58:59], s[58:59], 1
	v_lshl_add_u64 v[4:5], v[4:5], 0, s[58:59]
	s_lshl_b64 s[58:59], s[60:61], 1
	v_mul_u32_u24_e32 v2, s56, v164
	v_lshl_add_u64 v[4:5], v[4:5], 0, s[58:59]
	v_lshlrev_b32_e32 v2, 1, v2
	v_lshl_add_u64 v[4:5], v[4:5], 0, v[2:3]
	v_lshlrev_b32_e32 v2, 1, v162
	v_lshl_add_u64 v[4:5], v[4:5], 0, v[2:3]
	s_cmp_gt_u32 s44, 4
	s_cbranch_scc1 .Lgla_w21
	s_cmp_eq_u32 s44, 4
	s_cbranch_scc1 .Lgla_w20
	s_waitcnt vmcnt(10)
	s_branch .Lgla_wd
.Lgla_w20:
	s_waitcnt vmcnt(20)
	s_branch .Lgla_wd
.Lgla_w21:
	s_waitcnt vmcnt(21)
.Lgla_wd:
	v_cvt_pk_bf16_f32 v2, v74, v78
	v_cvt_pk_bf16_f32 v134, v86, v94
	v_cvt_pk_bf16_f32 v135, v102, v114
	v_cvt_pk_bf16_f32 v136, v126, v130
	v_cmp_gt_i32_e32 vcc, s63, v164
	s_lshl_b64 s[56:57], s[56:57], 1
	s_cmp_ge_i32 s44, s69
	v_cndmask_b32_e32 v137, 0, v136, vcc
	v_cndmask_b32_e32 v136, 0, v135, vcc
	v_cndmask_b32_e32 v135, 0, v134, vcc
	v_cndmask_b32_e32 v134, 0, v2, vcc
	global_store_dwordx4 v[4:5], v[134:137], off nt
	v_cvt_pk_bf16_f32 v2, v75, v79
	v_lshl_add_u64 v[4:5], v[4:5], 0, s[56:57]
	v_cvt_pk_bf16_f32 v134, v87, v95
	v_cvt_pk_bf16_f32 v135, v103, v115
	v_cvt_pk_bf16_f32 v136, v127, v131
	v_cndmask_b32_e32 v137, 0, v136, vcc
	v_cndmask_b32_e32 v136, 0, v135, vcc
	v_cndmask_b32_e32 v135, 0, v134, vcc
	v_cndmask_b32_e32 v134, 0, v2, vcc
	global_store_dwordx4 v[4:5], v[134:137], off nt
	v_cvt_pk_bf16_f32 v2, v76, v80
	v_lshl_add_u64 v[4:5], v[4:5], 0, s[56:57]
	v_cvt_pk_bf16_f32 v134, v88, v96
	v_cvt_pk_bf16_f32 v135, v104, v116
	v_cvt_pk_bf16_f32 v136, v128, v132
	v_cndmask_b32_e32 v137, 0, v136, vcc
	v_cndmask_b32_e32 v136, 0, v135, vcc
	v_cndmask_b32_e32 v135, 0, v134, vcc
	v_cndmask_b32_e32 v134, 0, v2, vcc
	global_store_dwordx4 v[4:5], v[134:137], off nt
	v_cvt_pk_bf16_f32 v2, v77, v81
	v_lshl_add_u64 v[4:5], v[4:5], 0, s[56:57]
	v_cvt_pk_bf16_f32 v134, v89, v97
	v_cvt_pk_bf16_f32 v135, v105, v117
	v_cvt_pk_bf16_f32 v136, v129, v133
	v_cndmask_b32_e32 v137, 0, v136, vcc
	v_cndmask_b32_e32 v136, 0, v135, vcc
	v_cndmask_b32_e32 v135, 0, v134, vcc
	v_cndmask_b32_e32 v134, 0, v2, vcc
	global_store_dwordx4 v[4:5], v[134:137], off nt
	s_cbranch_scc1 .LBB0_1681
	s_mul_i32 vcc_lo, s84, 0x228
	s_add_i32 vcc_lo, vcc_lo, s93
	s_min_i32 s90, vcc_lo, 0x324ff
	s_cmpk_gt_i32 vcc_lo, 0x19ff
	s_mov_b64 s[62:63], -1
	s_cbranch_scc0 .LBB0_1678
	s_cmpk_gt_u32 vcc_lo, 0x21ff
	s_cbranch_scc0 .LBB0_1675
	s_cmpk_gt_u32 vcc_lo, 0x4dff
	s_cbranch_scc0 .LBB0_1672
	s_cmpk_gt_u32 vcc_lo, 0x63ff
	s_cbranch_scc0 .LBB0_1669
	s_mov_b64 s[56:57], -1
	s_cmpk_gt_u32 vcc_lo, 0x7cff
	s_cbranch_scc0 .LBB0_1666
	s_cmpk_gt_u32 vcc_lo, 0x84ff
	s_cbranch_scc0 .LBB0_1663
	s_mov_b64 s[58:59], -1
	s_cmp_gt_u32 vcc_lo, 0x244ff
	s_mov_b64 s[60:61], -1
	s_cbranch_scc0 .LBB0_1661
	s_add_i32 s25, s90, 0xbb00
	s_bfe_u32 s46, s25, 0x6000a
	s_mulk_i32 s46, 0x2493
	s_lshr_b32 s46, s46, 16
	s_mul_i32 s52, s46, 0x1c00
	s_sub_i32 s25, s25, s52
	s_and_b32 s92, s25, 31
	s_bfe_u32 s91, s25, 0xb0005
	s_mov_b64 s[60:61], 0

; __device__ __forceinline__ void lds_barrier() { asm volatile("s_waitcnt lgkmcnt(0)" ::: "memory"); __builtin_amdgcn_s_barrier(); asm volatile("" ::: "memory"); }
; #define CT_LOADNT(T_) do { const int tt_ = (T_) < CT_TOTAL ? (T_) : CT_TOTAL - 1; const ConvTile ct_ = conv_tile_desc(cttab, tt_); const int ckq_ = lane >> 4, ccol_ = ((lane & 15) * 4 < ct_.nvalid) ? (lane & 15) * 4 : 0; CT_FORQ(CT_LOAD1NT) } while (0)
; #define CT_STORENT(T_) do { const int tt_ = (T_) < CT_TOTAL ? (T_) : CT_TOTAL - 1; const ConvTile ct_ = conv_tile_desc(cttab, tt_); const bool cok_ = (lane & 15) * 4 < ct_.nvalid; \
;     bf16_t* cdst_ = ct_.dst + (size_t)((lane & 15) * 4) * ct_.K + (lane >> 4) * 8; CT_ATOMNT(0, x) CT_ATOMNT(1, y) CT_ATOMNT(2, z) CT_ATOMNT(3, w) } while (0)
; __device__ __forceinline__ void ph_glascan(const Params& p, float* lds, int wg, int nwg, int gct_begin) {
;     ...
;             for (int ks = 0; ks < 2; ++ks) { cdec[ks] = ndec[ks];
; #pragma unroll
;                 for (int q = 0; q < 2; ++q) { ckh[ks][q] = nkh[ks][q]; cvt[ks][q] = nvt[ks][q]; } }
;             {
;                 const int tconv = gct_begin + c * (nwg * 8) + wg * 8 + w;
;                 if (c < gct_nch) { CT_STORENT(tconv); if (c + 1 < gct_nch) CT_LOADNT(tconv + nwg * 8); }
;             }
;             lds_barrier();
;         }
.LBB0_1680:
	s_lshl_b32 s61, s92, 6
	s_lshl_b32 s62, s92, 5
	s_and_b32 s62, s62, 0xffffff80
	s_and_b32 s63, s61, 64
	s_or_b32 s62, s62, s63
	s_bfe_u32 s63, s92, 0x10001
	s_and_b64 s[58:59], s[58:59], exec
	s_cselect_b32 s62, s61, s62
	s_cselect_b32 s63, 0, s63
	s_sub_i32 s61, s52, s61
	s_cmp_gt_i32 s61, 0
	s_cselect_b64 s[58:59], -1, 0
	s_or_b64 s[58:59], s[56:57], s[58:59]
	s_and_b64 s[56:57], s[56:57], exec
	s_cselect_b32 s61, 64, s61
	s_lshl_b32 s25, s25, 3
	s_add_i32 s25, s25, 0
	s_lshl_b32 s56, s63, 3
	s_add_i32 s25, s25, s56
	s_add_i32 s25, s25, 0x20040
	v_mov_b32_e32 v2, s25
	ds_read_b64 v[4:5], v2
	s_mul_i32 s25, s60, s46
	s_mul_hi_u32 s57, s25, s52
	s_mul_i32 s56, s25, s52
	s_lshl_b32 s25, s91, 5
	s_lshl_b64 s[56:57], s[56:57], 2
	s_ashr_i32 s46, s25, 31
	s_waitcnt lgkmcnt(0)
	v_lshl_add_u64 v[4:5], v[4:5], 0, s[56:57]
	s_mul_i32 s46, s52, s46
	s_mul_hi_u32 s56, s52, s25
	s_add_i32 s57, s56, s46
	s_mul_i32 s56, s52, s25
	s_lshl_b64 s[56:57], s[56:57], 2
	s_ashr_i32 s25, s62, 31
	v_lshl_add_u64 v[4:5], v[4:5], 0, s[56:57]
	s_and_b64 s[56:57], s[58:59], exec
	s_cselect_b32 s57, s25, 0
	s_cselect_b32 s56, s62, 0
	s_lshl_b64 s[56:57], s[56:57], 2
	v_mul_u32_u24_e32 v2, s52, v162
	v_lshl_add_u64 v[4:5], v[4:5], 0, s[56:57]
	v_lshlrev_b32_e32 v2, 2, v2
	v_cmp_gt_i32_e32 vcc, s61, v164
	v_mul_u32_u24_e32 v76, s52, v189
	v_mul_u32_u24_e32 v86, s52, v190
	v_mul_u32_u24_e32 v88, s52, v191
	v_mul_u32_u24_e32 v102, s52, v192
	v_mul_u32_u24_e32 v104, s52, v193
	v_mul_u32_u24_e32 v126, s52, v194
	v_lshl_add_u64 v[74:75], v[4:5], 0, v[2:3]
	v_cndmask_b32_e32 v2, 0, v164, vcc
	v_lshlrev_b32_e32 v76, 2, v76
	v_mov_b32_e32 v77, v3
	v_lshlrev_b32_e32 v86, 2, v86
	v_mov_b32_e32 v87, v3
	v_lshlrev_b32_e32 v88, 2, v88
	v_mov_b32_e32 v89, v3
	v_lshlrev_b32_e32 v102, 2, v102
	v_mov_b32_e32 v103, v3
	v_lshlrev_b32_e32 v104, 2, v104
	v_mov_b32_e32 v105, v3
	v_lshlrev_b32_e32 v126, 2, v126
	v_mov_b32_e32 v127, v3
	v_mul_u32_u24_e32 v128, s52, v195
	v_lshlrev_b32_e32 v2, 2, v2
	v_lshl_add_u64 v[76:77], v[4:5], 0, v[76:77]
	v_lshl_add_u64 v[86:87], v[4:5], 0, v[86:87]
	v_lshl_add_u64 v[88:89], v[4:5], 0, v[88:89]
	v_lshl_add_u64 v[102:103], v[4:5], 0, v[102:103]
	v_lshl_add_u64 v[104:105], v[4:5], 0, v[104:105]
	v_lshl_add_u64 v[126:127], v[4:5], 0, v[126:127]
	v_lshlrev_b32_e32 v128, 2, v128
	v_mov_b32_e32 v129, v3
	v_lshl_add_u64 v[74:75], v[74:75], 0, v[2:3]
	v_lshl_add_u64 v[78:79], v[76:77], 0, v[2:3]
	v_lshl_add_u64 v[86:87], v[86:87], 0, v[2:3]
	v_lshl_add_u64 v[94:95], v[88:89], 0, v[2:3]
	v_lshl_add_u64 v[102:103], v[102:103], 0, v[2:3]
	v_lshl_add_u64 v[114:115], v[104:105], 0, v[2:3]
	v_lshl_add_u64 v[126:127], v[126:127], 0, v[2:3]
	v_lshl_add_u64 v[4:5], v[4:5], 0, v[128:129]
	global_load_dwordx4 v[74:77], v[74:75], off nt
	s_nop 0
	global_load_dwordx4 v[78:81], v[78:79], off nt
	s_nop 0
	global_load_dwordx4 v[86:89], v[86:87], off nt
	s_nop 0
	global_load_dwordx4 v[94:97], v[94:95], off nt
	s_nop 0
	global_load_dwordx4 v[102:105], v[102:103], off nt
	s_nop 0
	global_load_dwordx4 v[114:117], v[114:115], off nt
	v_lshl_add_u64 v[4:5], v[4:5], 0, v[2:3]
	global_load_dwordx4 v[126:129], v[126:127], off nt
	s_nop 0
	global_load_dwordx4 v[130:133], v[4:5], off nt
.LBB0_1681:
	s_add_i32 s93, s93, s86
	s_waitcnt lgkmcnt(0)
	s_barrier
	s_add_u32 s54, s54, 0x8000
	s_addc_u32 s55, s55, 0
	s_mov_b64 s[56:57], 0x10000
	v_add_u32_e32 v206, 64, v206
	v_subrev_u32_e32 v175, 64, v175
	v_lshl_add_u64 v[176:177], v[176:177], 0, s[48:49]
	v_lshl_add_u64 v[178:179], v[178:179], 0, s[50:51]
	s_cmp_eq_u32 s54, 0x218000
	v_lshl_add_u64 v[186:187], v[186:187], 0, s[56:57]
	s_cbranch_scc1 .LBB0_1685
	s_cmp_lt_u32 s44, 4
	s_cbranch_scc1 .Lgla_t0
	s_waitcnt vmcnt(8)
	s_branch .Lgla_td

; __device__ __forceinline__ void ph_glascan(const Params& p, float* lds, int wg, int nwg, int gct_begin) {
;     ...
;             for (int ks = 0; ks < 2; ++ks) { cdec[ks] = ndec[ks];
; #pragma unroll
;                 for (int q = 0; q < 2; ++q) { ckh[ks][q] = nkh[ks][q]; cvt[ks][q] = nvt[ks][q]; } }
.Lgla_td:
	v_mov_b64_e32 v[144:145], v[120:121]
	v_mov_b64_e32 v[148:149], v[124:125]
	v_mov_b64_e32 v[136:137], v[112:113]
	v_mov_b64_e32 v[140:141], v[108:109]
	v_mov_b64_e32 v[142:143], v[118:119]
	v_mov_b64_e32 v[146:147], v[122:123]
	v_mov_b64_e32 v[134:135], v[110:111]
	v_mov_b64_e32 v[138:139], v[106:107]
	s_mov_b32 s90, s44
	s_branch .LBB0_1616
